# packed mLSTM output loop without the redundant s_nop padding between dependent packed FMAs
# speedup vs baseline: 1.0007x; 1.0004x over previous
; #define LAS __attribute__((address_space(3)))
; __device__ __forceinline__ bf16_t f2bf(float f) { unsigned u = __builtin_bit_cast(unsigned, f); return (bf16_t)((u + 0x7fffu + ((u >> 16) & 1u)) >> 16); }
; __device__ __forceinline__ int crow(int r, int hi) { return (r & 3) + 8 * (r >> 2) + 4 * hi; }
; __device__ __forceinline__ int crow(int r, int hi) { return (r & 3) + 8 * (r >> 2) + 4 * hi; }
; __device__ __forceinline__ void out_unit_m(LAS unsigned char* lds, LAS unsigned char* ldstab, const OutArgs a, const int wv) {
;     ...
;     __syncthreads();
;     constexpr int TP = DV * 2;
; #pragma unroll
;     for (int r = 0; r < 16; ++r) { const int row = 32 * rb + crow(r, hi);
;         const float inv = rsqrtf((s2[r] + exch[(1 - dh) * 128 + row]) * (1.f / DV) + EPS);
; #pragma unroll
;         for (int nb = 0; nb < 2; ++nb) *(LAS bf16_t*)(lds + row * TP + (dh * 64 + 32 * nb + r32) * 2) = f2bf(o[nb][r] * inv); }
.LBB0_648:
	s_or_b64 exec, exec, s[6:7]
	v_or_b32_e32 v56, s12, v156
	s_lshl_b32 s6, s8, 7
	v_subrev_u32_e32 v48, s6, v56
	s_add_i32 s7, 0, 0x22100
	v_lshl_add_u32 v48, v48, 2, s7
	s_waitcnt lgkmcnt(0)
	s_barrier
	ds_read_b128 v[48:51], v48 offset:512
	v_or_b32_e32 v57, 8, v56
	v_subrev_u32_e32 v52, s6, v57
	v_lshl_add_u32 v52, v52, 2, s7
	ds_read_b128 v[52:55], v52 offset:512
	s_waitcnt lgkmcnt(1)
	v_pk_add_f32 v[48:49], v[44:45], v[48:49]
	v_mov_b64_e32 v[44:45], s[46:47]
	v_pk_fma_f32 v[48:49], v[48:49], s[44:45], v[44:45] op_sel_hi:[1,0,0]
	v_lshlrev_b32_e32 v59, 1, v159
	v_mul_f32_e32 v58, 0x4b800000, v48
	v_cmp_gt_f32_e32 vcc, s83, v48
	s_add_i32 s8, s6, 0
	s_nop 0
	v_cndmask_b32_e32 v48, v48, v58, vcc
	v_rsq_f32_e32 v48, v48
	v_lshlrev_b32_e32 v58, 8, v56
	v_add3_u32 v58, s8, v58, v59
	v_mul_f32_e32 v60, 0x45800000, v48
	v_cndmask_b32_e32 v48, v48, v60, vcc
	v_mul_f32_e32 v0, v0, v48
	v_bfe_u32 v60, v0, 16, 1
	v_add3_u32 v0, v0, v60, s84
	ds_write_b16_d16_hi v58, v0
	v_mul_f32_e32 v0, v16, v48
	v_mul_f32_e32 v16, 0x4b800000, v49
	v_cmp_gt_f32_e32 vcc, s83, v49
	v_bfe_u32 v48, v0, 16, 1
	v_add3_u32 v0, v0, v48, s84
	v_cndmask_b32_e32 v16, v49, v16, vcc
	v_rsq_f32_e32 v16, v16
	ds_write_b16_d16_hi v58, v0 offset:64
	v_mul_f32_e32 v0, 0x45800000, v16
	v_cndmask_b32_e32 v0, v16, v0, vcc
	v_mul_f32_e32 v1, v1, v0
	v_bfe_u32 v16, v1, 16, 1
	v_add3_u32 v1, v1, v16, s84
	ds_write_b16_d16_hi v58, v1 offset:256
	v_mul_f32_e32 v16, v17, v0
	v_pk_add_f32 v[0:1], v[46:47], v[50:51]
	s_nop 0
	v_pk_fma_f32 v[0:1], v[0:1], s[44:45], v[44:45] op_sel_hi:[1,0,0]
	s_nop 0
	v_mul_f32_e32 v17, 0x4b800000, v0
	v_cmp_gt_f32_e32 vcc, s83, v0
	s_nop 1
	v_cndmask_b32_e32 v0, v0, v17, vcc
	v_rsq_f32_e32 v0, v0
	v_bfe_u32 v17, v16, 16, 1
	v_add3_u32 v16, v16, v17, s84
	ds_write_b16_d16_hi v58, v16 offset:320
	v_mul_f32_e32 v16, 0x45800000, v0
	v_cndmask_b32_e32 v0, v0, v16, vcc
	v_mul_f32_e32 v2, v2, v0
	v_bfe_u32 v16, v2, 16, 1
	v_add3_u32 v2, v2, v16, s84
	ds_write_b16_d16_hi v58, v2 offset:512
	v_mul_f32_e32 v2, 0x4b800000, v1
	v_cmp_gt_f32_e32 vcc, s83, v1
	v_mul_f32_e32 v0, v18, v0
	v_or_b32_e32 v17, 16, v56
	v_cndmask_b32_e32 v1, v1, v2, vcc
	v_rsq_f32_e32 v1, v1
	v_bfe_u32 v2, v0, 16, 1
	v_add3_u32 v0, v0, v2, s84
	ds_write_b16_d16_hi v58, v0 offset:576
	v_mul_f32_e32 v0, 0x45800000, v1
	v_cndmask_b32_e32 v0, v1, v0, vcc
	v_mul_f32_e32 v1, v3, v0
	v_bfe_u32 v2, v1, 16, 1
	v_add3_u32 v1, v1, v2, s84
	v_mul_f32_e32 v0, v19, v0
	ds_write_b16_d16_hi v58, v1 offset:768
	v_bfe_u32 v1, v0, 16, 1
	v_add3_u32 v2, v0, v1, s84
	s_waitcnt lgkmcnt(7)
	v_pk_add_f32 v[0:1], v[40:41], v[52:53]
	ds_write_b16_d16_hi v58, v2 offset:832
	v_pk_fma_f32 v[0:1], v[0:1], s[44:45], v[44:45] op_sel_hi:[1,0,0]
	v_lshlrev_b32_e32 v2, 8, v57
	v_mul_f32_e32 v3, 0x4b800000, v0
	v_cmp_gt_f32_e32 vcc, s83, v0
	v_add3_u32 v2, s8, v2, v59
	v_or_b32_e32 v18, 24, v56
	v_cndmask_b32_e32 v0, v0, v3, vcc
	v_rsq_f32_e32 v0, v0
	s_nop 0
	v_mul_f32_e32 v3, 0x45800000, v0
	v_cndmask_b32_e32 v0, v0, v3, vcc
	v_mul_f32_e32 v3, v4, v0
	v_bfe_u32 v4, v3, 16, 1
	v_add3_u32 v3, v3, v4, s84
	ds_write_b16_d16_hi v2, v3
	v_mul_f32_e32 v3, 0x4b800000, v1
	v_cmp_gt_f32_e32 vcc, s83, v1
	v_mul_f32_e32 v0, v20, v0
	v_subrev_u32_e32 v4, s6, v18
	v_cndmask_b32_e32 v1, v1, v3, vcc
	v_rsq_f32_e32 v1, v1
	v_bfe_u32 v3, v0, 16, 1
	v_add3_u32 v0, v0, v3, s84
	ds_write_b16_d16_hi v2, v0 offset:64
	v_mul_f32_e32 v0, 0x45800000, v1
	v_cndmask_b32_e32 v0, v1, v0, vcc
	v_mul_f32_e32 v1, v5, v0
	v_bfe_u32 v2, v1, 16, 1
	v_add3_u32 v1, v1, v2, s84
	ds_write_b16_d16_hi v58, v1 offset:2304
	v_mul_f32_e32 v2, v21, v0
	v_pk_add_f32 v[0:1], v[42:43], v[54:55]
	v_lshl_add_u32 v4, v4, 2, s7
	v_pk_fma_f32 v[0:1], v[0:1], s[44:45], v[44:45] op_sel_hi:[1,0,0]
	s_nop 0
	v_mul_f32_e32 v3, 0x4b800000, v0
	v_cmp_gt_f32_e32 vcc, s83, v0
	s_nop 1
	v_cndmask_b32_e32 v0, v0, v3, vcc
	v_rsq_f32_e32 v0, v0
	v_bfe_u32 v3, v2, 16, 1
	v_add3_u32 v2, v2, v3, s84
	ds_write_b16_d16_hi v58, v2 offset:2368
	v_mul_f32_e32 v2, 0x45800000, v0
	v_cndmask_b32_e32 v0, v0, v2, vcc
	v_mul_f32_e32 v2, v6, v0
	v_bfe_u32 v3, v2, 16, 1
	v_add3_u32 v2, v2, v3, s84
	ds_write_b16_d16_hi v58, v2 offset:2560
	v_mul_f32_e32 v2, 0x4b800000, v1
	v_cmp_gt_f32_e32 vcc, s83, v1
	v_mul_f32_e32 v0, v22, v0
	s_nop 0
	v_cndmask_b32_e32 v1, v1, v2, vcc
	v_rsq_f32_e32 v1, v1
	v_bfe_u32 v2, v0, 16, 1
	v_add3_u32 v0, v0, v2, s84
	ds_write_b16_d16_hi v58, v0 offset:2624
	v_mul_f32_e32 v0, 0x45800000, v1
	v_cndmask_b32_e32 v0, v1, v0, vcc
	v_mul_f32_e32 v1, v7, v0
	v_bfe_u32 v2, v1, 16, 1
	v_add3_u32 v1, v1, v2, s84
	v_mul_f32_e32 v0, v23, v0
	ds_write_b16_d16_hi v58, v1 offset:2816
	v_bfe_u32 v1, v0, 16, 1
	v_add3_u32 v16, v0, v1, s84
	v_subrev_u32_e32 v0, s6, v17
	v_lshl_add_u32 v0, v0, 2, s7
	ds_read_b128 v[0:3], v0 offset:512
	ds_read_b128 v[4:7], v4 offset:512
	ds_write_b16_d16_hi v58, v16 offset:2880
	v_lshlrev_b32_e32 v16, 8, v17
	v_add3_u32 v16, s8, v16, v59
	s_waitcnt lgkmcnt(2)
; #define LAS __attribute__((address_space(3)))
; __device__ __forceinline__ bf16_t f2bf(float f) { unsigned u = __builtin_bit_cast(unsigned, f); return (bf16_t)((u + 0x7fffu + ((u >> 16) & 1u)) >> 16); }
; __device__ __forceinline__ int crow(int r, int hi) { return (r & 3) + 8 * (r >> 2) + 4 * hi; }
; __device__ __forceinline__ int crow(int r, int hi) { return (r & 3) + 8 * (r >> 2) + 4 * hi; }
; __device__ __forceinline__ void out_unit_m(LAS unsigned char* lds, LAS unsigned char* ldstab, const OutArgs a, const int wv) {
;     ...
;     __syncthreads();
;     constexpr int TP = DV * 2;
; #pragma unroll
;     for (int r = 0; r < 16; ++r) { const int row = 32 * rb + crow(r, hi);
;         const float inv = rsqrtf((s2[r] + exch[(1 - dh) * 128 + row]) * (1.f / DV) + EPS);
; #pragma unroll
;         for (int nb = 0; nb < 2; ++nb) *(LAS bf16_t*)(lds + row * TP + (dh * 64 + 32 * nb + r32) * 2) = f2bf(o[nb][r] * inv); }
;     __syncthreads();
; #pragma unroll 1
;     for (int id = tid; id < 128 * 16; id += 512) { const int row = id >> 4, ch = id & 15;
;         const u32x4 y = *(const LAS u32x4*)(lds + row * TP + ch * 16); const u32x4 g = *(const u32x4*)(a.G + (size_t)row * a.ldg + 8 * ch);
;         const f32x4 g0 = *(const f32x4*)(a.gain + 8 * ch), g1 = *(const f32x4*)(a.gain + 8 * ch + 4);
;         const float yv[8] = {bf_lo(y.x), bf_hi(y.x), bf_lo(y.y), bf_hi(y.y), bf_lo(y.z), bf_hi(y.z), bf_lo(y.w), bf_hi(y.w)};
;         const float gv[8] = {bf_lo(g.x), bf_hi(g.x), bf_lo(g.y), bf_hi(g.y), bf_lo(g.z), bf_hi(g.z), bf_lo(g.w), bf_hi(g.w)};
	v_pk_add_f32 v[0:1], v[36:37], v[0:1]
	s_nop 0
	v_pk_fma_f32 v[0:1], v[0:1], s[44:45], v[44:45] op_sel_hi:[1,0,0]
	s_nop 0
	v_mul_f32_e32 v19, 0x4b800000, v0
	v_cmp_gt_f32_e32 vcc, s83, v0
	s_nop 1
	v_cndmask_b32_e32 v0, v0, v19, vcc
	v_rsq_f32_e32 v0, v0
	s_nop 0
	v_mul_f32_e32 v17, 0x45800000, v0
	v_cndmask_b32_e32 v0, v0, v17, vcc
	v_mul_f32_e32 v8, v8, v0
	v_bfe_u32 v17, v8, 16, 1
	v_add3_u32 v8, v8, v17, s84
	ds_write_b16_d16_hi v16, v8
	v_mul_f32_e32 v8, 0x4b800000, v1
	v_cmp_gt_f32_e32 vcc, s83, v1
	v_mul_f32_e32 v0, v24, v0
	s_nop 0
	v_cndmask_b32_e32 v1, v1, v8, vcc
	v_rsq_f32_e32 v1, v1
	v_bfe_u32 v8, v0, 16, 1
	v_add3_u32 v0, v0, v8, s84
	ds_write_b16_d16_hi v16, v0 offset:64
	v_mul_f32_e32 v0, 0x45800000, v1
	v_cndmask_b32_e32 v0, v1, v0, vcc
	v_mul_f32_e32 v1, v9, v0
	v_bfe_u32 v8, v1, 16, 1
	v_add3_u32 v1, v1, v8, s84
	ds_write_b16_d16_hi v58, v1 offset:4352
	v_mul_f32_e32 v8, v25, v0
	v_pk_add_f32 v[0:1], v[38:39], v[2:3]
	s_nop 0
	v_pk_fma_f32 v[0:1], v[0:1], s[44:45], v[44:45] op_sel_hi:[1,0,0]
	s_nop 0
	v_mul_f32_e32 v2, 0x4b800000, v0
	v_cmp_gt_f32_e32 vcc, s83, v0
	s_nop 1
	v_cndmask_b32_e32 v0, v0, v2, vcc
	v_rsq_f32_e32 v0, v0
	v_bfe_u32 v2, v8, 16, 1
	v_add3_u32 v2, v8, v2, s84
	ds_write_b16_d16_hi v58, v2 offset:4416
	v_mul_f32_e32 v2, 0x45800000, v0
	v_cndmask_b32_e32 v0, v0, v2, vcc
	v_mul_f32_e32 v2, v10, v0
	v_bfe_u32 v3, v2, 16, 1
	v_add3_u32 v2, v2, v3, s84
	ds_write_b16_d16_hi v58, v2 offset:4608
	v_mul_f32_e32 v2, 0x4b800000, v1
	v_cmp_gt_f32_e32 vcc, s83, v1
	v_mul_f32_e32 v0, v26, v0
	s_nop 0
	v_cndmask_b32_e32 v1, v1, v2, vcc
	v_rsq_f32_e32 v1, v1
	v_bfe_u32 v2, v0, 16, 1
	v_add3_u32 v0, v0, v2, s84
	ds_write_b16_d16_hi v58, v0 offset:4672
	v_mul_f32_e32 v0, 0x45800000, v1
	v_cndmask_b32_e32 v0, v1, v0, vcc
	v_mul_f32_e32 v1, v11, v0
	v_bfe_u32 v2, v1, 16, 1
	v_add3_u32 v1, v1, v2, s84
	v_mul_f32_e32 v0, v27, v0
	ds_write_b16_d16_hi v58, v1 offset:4864
	v_bfe_u32 v1, v0, 16, 1
	v_add3_u32 v2, v0, v1, s84
	s_waitcnt lgkmcnt(8)
	v_pk_add_f32 v[0:1], v[32:33], v[4:5]
	ds_write_b16_d16_hi v58, v2 offset:4928
	v_pk_fma_f32 v[0:1], v[0:1], s[44:45], v[44:45] op_sel_hi:[1,0,0]
	v_lshlrev_b32_e32 v2, 8, v18
	v_mul_f32_e32 v3, 0x4b800000, v0
	v_cmp_gt_f32_e32 vcc, s83, v0
	v_add3_u32 v2, s8, v2, v59
	s_nop 0
	v_cndmask_b32_e32 v0, v0, v3, vcc
	v_rsq_f32_e32 v0, v0
	s_nop 0
	v_mul_f32_e32 v3, 0x45800000, v0
	v_cndmask_b32_e32 v0, v0, v3, vcc
	v_mul_f32_e32 v3, v12, v0
	v_bfe_u32 v4, v3, 16, 1
	v_add3_u32 v3, v3, v4, s84
	ds_write_b16_d16_hi v2, v3
	v_mul_f32_e32 v3, 0x4b800000, v1
	v_cmp_gt_f32_e32 vcc, s83, v1
	v_mul_f32_e32 v0, v28, v0
	s_nop 0
	v_cndmask_b32_e32 v1, v1, v3, vcc
	v_rsq_f32_e32 v1, v1
	v_bfe_u32 v3, v0, 16, 1
	v_add3_u32 v0, v0, v3, s84
	ds_write_b16_d16_hi v2, v0 offset:64
	v_mul_f32_e32 v0, 0x45800000, v1
	v_cndmask_b32_e32 v0, v1, v0, vcc
	v_mul_f32_e32 v1, v13, v0
	v_bfe_u32 v2, v1, 16, 1
	v_add3_u32 v1, v1, v2, s84
	ds_write_b16_d16_hi v58, v1 offset:6400
	v_mul_f32_e32 v2, v29, v0
	v_pk_add_f32 v[0:1], v[34:35], v[6:7]
	s_nop 0
	v_pk_fma_f32 v[0:1], v[0:1], s[44:45], v[44:45] op_sel_hi:[1,0,0]
	s_nop 0
	v_mul_f32_e32 v3, 0x4b800000, v0
	v_cmp_gt_f32_e32 vcc, s83, v0
	s_nop 1
	v_cndmask_b32_e32 v0, v0, v3, vcc
	v_rsq_f32_e32 v0, v0
	v_bfe_u32 v3, v2, 16, 1
	v_add3_u32 v2, v2, v3, s84
	ds_write_b16_d16_hi v58, v2 offset:6464
	v_mul_f32_e32 v2, 0x45800000, v0
	v_cndmask_b32_e32 v0, v0, v2, vcc
	v_mul_f32_e32 v2, v14, v0
	v_bfe_u32 v3, v2, 16, 1
	v_add3_u32 v2, v2, v3, s84
	ds_write_b16_d16_hi v58, v2 offset:6656
	v_mul_f32_e32 v2, 0x4b800000, v1
	v_cmp_gt_f32_e32 vcc, s83, v1
	v_mul_f32_e32 v0, v30, v0
	s_nop 0
	v_cndmask_b32_e32 v1, v1, v2, vcc
	v_rsq_f32_e32 v1, v1
	v_bfe_u32 v2, v0, 16, 1
	v_add3_u32 v0, v0, v2, s84
	ds_write_b16_d16_hi v58, v0 offset:6720
	v_mul_f32_e32 v0, 0x45800000, v1
	v_cndmask_b32_e32 v0, v1, v0, vcc
	v_mul_f32_e32 v1, v15, v0
	v_bfe_u32 v2, v1, 16, 1
	v_add3_u32 v1, v1, v2, s84
	v_mul_f32_e32 v0, v31, v0
	ds_write_b16_d16_hi v58, v1 offset:6912
	v_bfe_u32 v1, v0, 16, 1
	v_add3_u32 v0, v0, v1, s84
	v_cmp_gt_i32_e32 vcc, s85, v158
	ds_write_b16_d16_hi v58, v0 offset:6976
	s_waitcnt lgkmcnt(0)
	s_barrier
	s_and_saveexec_b64 s[48:49], vcc
	s_cbranch_execz .LBB0_651
	s_lshl_b64 s[6:7], s[40:41], 2
	s_add_u32 s4, s4, s6
	s_addc_u32 s5, s5, s7
	s_add_u32 s6, s65, s89
	s_addc_u32 s7, s66, 0
	s_add_u32 s6, s6, s40
	v_and_b32_e32 v2, 15, v158
	s_addc_u32 s7, s7, 0
	v_lshlrev_b32_e32 v0, 4, v2
	v_lshlrev_b32_e32 v156, 3, v2
	v_mov_b32_e32 v1, v157
	v_lshlrev_b32_e32 v2, 5, v2
	v_mov_b32_e32 v3, v157
	v_add_u32_e32 v8, 0, v0
	v_lshl_add_u64 v[0:1], v[160:161], 0, v[0:1]
	v_lshl_add_u64 v[2:3], s[4:5], 0, v[2:3]
	v_lshl_add_u64 v[4:5], s[6:7], 0, v[156:157]
	s_mov_b64 s[50:51], 0
	s_mov_b32 s98, 0xbfb8aa3b
	s_mov_b32 s100, 0x41800000
	v_ashrrev_i32_e32 v6, 4, v158
	global_load_dwordx4 v[36:39], v[2:3], off offset:16
	global_load_dwordx4 v[32:35], v[2:3], off
	v_mad_i64_i32 v[18:19], s[4:5], v6, s71, v[0:1]
	global_load_dwordx4 v[40:43], v[18:19], off offset:3072
	v_add_u32_e32 v9, 32, v6
	v_mad_i64_i32 v[20:21], s[4:5], v9, s71, v[0:1]
	global_load_dwordx4 v[44:47], v[20:21], off offset:3072
	v_add_u32_e32 v9, 64, v6
	v_mad_i64_i32 v[18:19], s[4:5], v9, s71, v[0:1]
	global_load_dwordx4 v[48:51], v[18:19], off offset:3072
	v_add_u32_e32 v9, 96, v6
	v_mad_i64_i32 v[20:21], s[4:5], v9, s71, v[0:1]
	global_load_dwordx4 v[52:55], v[20:21], off offset:3072
	v_lshl_add_u32 v7, v6, 8, v8
	ds_read_b128 v[22:25], v7
	s_waitcnt vmcnt(3) lgkmcnt(0)
; #define LAS __attribute__((address_space(3)))
; __device__ __forceinline__ float sigmoidf_(float x) { return 1.f / (1.f + __expf(-x)); }
; __device__ __forceinline__ unsigned pk4_fp8c(float a, float b, float c, float d) { return pk4_fp8(__builtin_amdgcn_fmed3f(a, -448.f, 448.f), __builtin_amdgcn_fmed3f(b, -448.f, 448.f), __builtin_amdgcn_fmed3f(c, -448.f, 448.f), __builtin_amdgcn_fmed3f(d, -448.f, 448.f)); }
; __device__ __forceinline__ void out_unit_m(LAS unsigned char* lds, LAS unsigned char* ldstab, const OutArgs a, const int wv) {
;     ...
;     for (int id = tid; id < 128 * 16; id += 512) { const int row = id >> 4, ch = id & 15;
;         const u32x4 y = *(const LAS u32x4*)(lds + row * TP + ch * 16); const u32x4 g = *(const u32x4*)(a.G + (size_t)row * a.ldg + 8 * ch);
;         const f32x4 g0 = *(const f32x4*)(a.gain + 8 * ch), g1 = *(const f32x4*)(a.gain + 8 * ch + 4);
;         const float yv[8] = {bf_lo(y.x), bf_hi(y.x), bf_lo(y.y), bf_hi(y.y), bf_lo(y.z), bf_hi(y.z), bf_lo(y.w), bf_hi(y.w)};
;         const float gv[8] = {bf_lo(g.x), bf_hi(g.x), bf_lo(g.y), bf_hi(g.y), bf_lo(g.z), bf_hi(g.z), bf_lo(g.w), bf_hi(g.w)};
;         const float gn[8] = {g0[0], g0[1], g0[2], g0[3], g1[0], g1[1], g1[2], g1[3]};
;         float ov[8];
; #pragma unroll
;         for (int i = 0; i < 8; ++i) ov[i] = yv[i] * gn[i] * sigmoidf_(gv[i]);
;         u32x2 w; w.x = pg8::pk4_fp8c(ov[0] * a.oscale, ov[1] * a.oscale, ov[2] * a.oscale, ov[3] * a.oscale); w.y = pg8::pk4_fp8c(ov[4] * a.oscale, ov[5] * a.oscale, ov[6] * a.oscale, ov[7] * a.oscale);
;         *(u32x2*)(a.Out + (size_t)row * a.ldo + 8 * ch) = w; }
	v_lshlrev_b32_e32 v10, 16, v22
	v_and_b32_e32 v11, 0xffff0000, v22
	v_lshlrev_b32_e32 v12, 16, v23
	v_and_b32_e32 v13, 0xffff0000, v23
	v_lshlrev_b32_e32 v14, 16, v24
	v_and_b32_e32 v15, 0xffff0000, v24
	v_lshlrev_b32_e32 v16, 16, v25
	v_and_b32_e32 v17, 0xffff0000, v25
	v_pk_mul_f32 v[10:11], v[32:33], v[10:11]
	v_pk_mul_f32 v[12:13], v[34:35], v[12:13]
	v_pk_mul_f32 v[14:15], v[36:37], v[14:15]
	v_pk_mul_f32 v[16:17], v[38:39], v[16:17]
	v_lshlrev_b32_e32 v56, 16, v40
	v_and_b32_e32 v57, 0xffff0000, v40
	v_lshlrev_b32_e32 v58, 16, v41
	v_and_b32_e32 v59, 0xffff0000, v41
	v_pk_mul_f32 v[56:57], v[56:57], s[98:99] op_sel_hi:[1,0]
	v_pk_mul_f32 v[58:59], v[58:59], s[98:99] op_sel_hi:[1,0]
	v_exp_f32_e32 v56, v56
	v_exp_f32_e32 v57, v57
	v_exp_f32_e32 v58, v58
	v_exp_f32_e32 v59, v59
	v_pk_add_f32 v[56:57], v[56:57], 1.0 op_sel_hi:[1,0]
	v_pk_add_f32 v[58:59], v[58:59], 1.0 op_sel_hi:[1,0]
	v_rcp_f32_e32 v60, v56
	v_rcp_f32_e32 v61, v57
	v_rcp_f32_e32 v62, v58
	v_rcp_f32_e32 v63, v59
	v_pk_fma_f32 v[28:29], v[56:57], v[60:61], 1.0 op_sel_hi:[1,1,0] neg_lo:[1,0,0] neg_hi:[1,0,0]
	v_pk_fma_f32 v[30:31], v[58:59], v[62:63], 1.0 op_sel_hi:[1,1,0] neg_lo:[1,0,0] neg_hi:[1,0,0]
	v_pk_fma_f32 v[60:61], v[28:29], v[60:61], v[60:61]
	v_pk_fma_f32 v[62:63], v[30:31], v[62:63], v[62:63]
	v_pk_fma_f32 v[28:29], v[56:57], v[60:61], 1.0 op_sel_hi:[1,1,0] neg_lo:[1,0,0] neg_hi:[1,0,0]
	v_pk_fma_f32 v[30:31], v[58:59], v[62:63], 1.0 op_sel_hi:[1,1,0] neg_lo:[1,0,0] neg_hi:[1,0,0]
	v_pk_fma_f32 v[64:65], v[28:29], v[60:61], v[60:61]
	v_pk_fma_f32 v[66:67], v[30:31], v[62:63], v[62:63]
	v_pk_fma_f32 v[28:29], v[56:57], v[64:65], 1.0 op_sel_hi:[1,1,0] neg_lo:[1,0,0] neg_hi:[1,0,0]
	v_pk_fma_f32 v[30:31], v[58:59], v[66:67], 1.0 op_sel_hi:[1,1,0] neg_lo:[1,0,0] neg_hi:[1,0,0]
	v_pk_fma_f32 v[28:29], v[28:29], v[60:61], v[64:65]
	v_pk_fma_f32 v[30:31], v[30:31], v[62:63], v[66:67]
	v_div_fixup_f32 v28, v28, v56, 1.0
	v_div_fixup_f32 v29, v29, v57, 1.0
	v_div_fixup_f32 v30, v30, v58, 1.0
	v_div_fixup_f32 v31, v31, v59, 1.0
	v_pk_mul_f32 v[10:11], v[10:11], v[28:29]
	v_pk_mul_f32 v[12:13], v[12:13], v[30:31]
	v_lshlrev_b32_e32 v56, 16, v42
	v_and_b32_e32 v57, 0xffff0000, v42
	v_lshlrev_b32_e32 v58, 16, v43
	v_and_b32_e32 v59, 0xffff0000, v43
	v_pk_mul_f32 v[56:57], v[56:57], s[98:99] op_sel_hi:[1,0]
	v_pk_mul_f32 v[58:59], v[58:59], s[98:99] op_sel_hi:[1,0]
	v_exp_f32_e32 v56, v56
	v_exp_f32_e32 v57, v57
	v_exp_f32_e32 v58, v58
	v_exp_f32_e32 v59, v59
	v_pk_add_f32 v[56:57], v[56:57], 1.0 op_sel_hi:[1,0]
	v_pk_add_f32 v[58:59], v[58:59], 1.0 op_sel_hi:[1,0]
	v_rcp_f32_e32 v60, v56
	v_rcp_f32_e32 v61, v57
	v_rcp_f32_e32 v62, v58
	v_rcp_f32_e32 v63, v59
	v_pk_fma_f32 v[28:29], v[56:57], v[60:61], 1.0 op_sel_hi:[1,1,0] neg_lo:[1,0,0] neg_hi:[1,0,0]
	v_pk_fma_f32 v[30:31], v[58:59], v[62:63], 1.0 op_sel_hi:[1,1,0] neg_lo:[1,0,0] neg_hi:[1,0,0]
	v_pk_fma_f32 v[60:61], v[28:29], v[60:61], v[60:61]
	v_pk_fma_f32 v[62:63], v[30:31], v[62:63], v[62:63]
	v_pk_fma_f32 v[28:29], v[56:57], v[60:61], 1.0 op_sel_hi:[1,1,0] neg_lo:[1,0,0] neg_hi:[1,0,0]
	v_pk_fma_f32 v[30:31], v[58:59], v[62:63], 1.0 op_sel_hi:[1,1,0] neg_lo:[1,0,0] neg_hi:[1,0,0]
	v_pk_fma_f32 v[64:65], v[28:29], v[60:61], v[60:61]
	v_pk_fma_f32 v[66:67], v[30:31], v[62:63], v[62:63]
	v_pk_fma_f32 v[28:29], v[56:57], v[64:65], 1.0 op_sel_hi:[1,1,0] neg_lo:[1,0,0] neg_hi:[1,0,0]
	v_pk_fma_f32 v[30:31], v[58:59], v[66:67], 1.0 op_sel_hi:[1,1,0] neg_lo:[1,0,0] neg_hi:[1,0,0]
	v_pk_fma_f32 v[28:29], v[28:29], v[60:61], v[64:65]
	v_pk_fma_f32 v[30:31], v[30:31], v[62:63], v[66:67]
	v_div_fixup_f32 v28, v28, v56, 1.0
	v_div_fixup_f32 v29, v29, v57, 1.0
	v_div_fixup_f32 v30, v30, v58, 1.0
	v_div_fixup_f32 v31, v31, v59, 1.0
	v_pk_mul_f32 v[14:15], v[14:15], v[28:29]
	v_pk_mul_f32 v[16:17], v[16:17], v[30:31]
	v_pk_mul_f32 v[10:11], v[10:11], s[100:101] op_sel_hi:[1,0]
	v_pk_mul_f32 v[12:13], v[12:13], s[100:101] op_sel_hi:[1,0]
	v_pk_mul_f32 v[14:15], v[14:15], s[100:101] op_sel_hi:[1,0]
	v_pk_mul_f32 v[16:17], v[16:17], s[100:101] op_sel_hi:[1,0]
	v_med3_f32 v10, v10, s86, v202
	v_med3_f32 v11, v11, s86, v202
	v_med3_f32 v12, v12, s86, v202
	v_med3_f32 v13, v13, s86, v202
	v_med3_f32 v14, v14, s86, v202
	v_med3_f32 v15, v15, s86, v202
	v_med3_f32 v16, v16, s86, v202
	v_med3_f32 v17, v17, s86, v202
	v_mov_b32_e32 v20, v6
	v_mov_b32_e32 v21, 0
	v_cvt_pk_fp8_f32 v26, v10, v11
	v_cvt_pk_fp8_f32 v27, v14, v15
	v_lshlrev_b64 v[20:21], 10, v[20:21]
	v_cvt_pk_fp8_f32 v26, v12, v13 op_sel:[0,0,1]
	v_cvt_pk_fp8_f32 v27, v16, v17 op_sel:[0,0,1]
	v_lshl_add_u64 v[20:21], v[4:5], 0, v[20:21]
	s_nop 0
	global_store_dwordx2 v[20:21], v[26:27], off
	v_add_u32_e32 v9, 32, v6
	v_lshl_add_u32 v7, v9, 8, v8
	ds_read_b128 v[22:25], v7
	s_waitcnt vmcnt(3) lgkmcnt(0)
; #define LAS __attribute__((address_space(3)))
; __device__ __forceinline__ float sigmoidf_(float x) { return 1.f / (1.f + __expf(-x)); }
; __device__ __forceinline__ unsigned pk4_fp8c(float a, float b, float c, float d) { return pk4_fp8(__builtin_amdgcn_fmed3f(a, -448.f, 448.f), __builtin_amdgcn_fmed3f(b, -448.f, 448.f), __builtin_amdgcn_fmed3f(c, -448.f, 448.f), __builtin_amdgcn_fmed3f(d, -448.f, 448.f)); }
; __device__ __forceinline__ void out_unit_m(LAS unsigned char* lds, LAS unsigned char* ldstab, const OutArgs a, const int wv) {
;     ...
;     for (int id = tid; id < 128 * 16; id += 512) { const int row = id >> 4, ch = id & 15;
;         const u32x4 y = *(const LAS u32x4*)(lds + row * TP + ch * 16); const u32x4 g = *(const u32x4*)(a.G + (size_t)row * a.ldg + 8 * ch);
;         const f32x4 g0 = *(const f32x4*)(a.gain + 8 * ch), g1 = *(const f32x4*)(a.gain + 8 * ch + 4);
;         const float yv[8] = {bf_lo(y.x), bf_hi(y.x), bf_lo(y.y), bf_hi(y.y), bf_lo(y.z), bf_hi(y.z), bf_lo(y.w), bf_hi(y.w)};
;         const float gv[8] = {bf_lo(g.x), bf_hi(g.x), bf_lo(g.y), bf_hi(g.y), bf_lo(g.z), bf_hi(g.z), bf_lo(g.w), bf_hi(g.w)};
;         const float gn[8] = {g0[0], g0[1], g0[2], g0[3], g1[0], g1[1], g1[2], g1[3]};
;         float ov[8];
; #pragma unroll
;         for (int i = 0; i < 8; ++i) ov[i] = yv[i] * gn[i] * sigmoidf_(gv[i]);
;         u32x2 w; w.x = pg8::pk4_fp8c(ov[0] * a.oscale, ov[1] * a.oscale, ov[2] * a.oscale, ov[3] * a.oscale); w.y = pg8::pk4_fp8c(ov[4] * a.oscale, ov[5] * a.oscale, ov[6] * a.oscale, ov[7] * a.oscale);
;         *(u32x2*)(a.Out + (size_t)row * a.ldo + 8 * ch) = w; }
	v_lshlrev_b32_e32 v10, 16, v22
	v_and_b32_e32 v11, 0xffff0000, v22
	v_lshlrev_b32_e32 v12, 16, v23
	v_and_b32_e32 v13, 0xffff0000, v23
	v_lshlrev_b32_e32 v14, 16, v24
	v_and_b32_e32 v15, 0xffff0000, v24
	v_lshlrev_b32_e32 v16, 16, v25
	v_and_b32_e32 v17, 0xffff0000, v25
	v_pk_mul_f32 v[10:11], v[32:33], v[10:11]
	v_pk_mul_f32 v[12:13], v[34:35], v[12:13]
	v_pk_mul_f32 v[14:15], v[36:37], v[14:15]
	v_pk_mul_f32 v[16:17], v[38:39], v[16:17]
	v_lshlrev_b32_e32 v56, 16, v44
	v_and_b32_e32 v57, 0xffff0000, v44
	v_lshlrev_b32_e32 v58, 16, v45
	v_and_b32_e32 v59, 0xffff0000, v45
	v_pk_mul_f32 v[56:57], v[56:57], s[98:99] op_sel_hi:[1,0]
	v_pk_mul_f32 v[58:59], v[58:59], s[98:99] op_sel_hi:[1,0]
	v_exp_f32_e32 v56, v56
	v_exp_f32_e32 v57, v57
	v_exp_f32_e32 v58, v58
	v_exp_f32_e32 v59, v59
	v_pk_add_f32 v[56:57], v[56:57], 1.0 op_sel_hi:[1,0]
	v_pk_add_f32 v[58:59], v[58:59], 1.0 op_sel_hi:[1,0]
	v_rcp_f32_e32 v60, v56
	v_rcp_f32_e32 v61, v57
	v_rcp_f32_e32 v62, v58
	v_rcp_f32_e32 v63, v59
	v_pk_fma_f32 v[28:29], v[56:57], v[60:61], 1.0 op_sel_hi:[1,1,0] neg_lo:[1,0,0] neg_hi:[1,0,0]
	v_pk_fma_f32 v[30:31], v[58:59], v[62:63], 1.0 op_sel_hi:[1,1,0] neg_lo:[1,0,0] neg_hi:[1,0,0]
	v_pk_fma_f32 v[60:61], v[28:29], v[60:61], v[60:61]
	v_pk_fma_f32 v[62:63], v[30:31], v[62:63], v[62:63]
	v_pk_fma_f32 v[28:29], v[56:57], v[60:61], 1.0 op_sel_hi:[1,1,0] neg_lo:[1,0,0] neg_hi:[1,0,0]
	v_pk_fma_f32 v[30:31], v[58:59], v[62:63], 1.0 op_sel_hi:[1,1,0] neg_lo:[1,0,0] neg_hi:[1,0,0]
	v_pk_fma_f32 v[64:65], v[28:29], v[60:61], v[60:61]
	v_pk_fma_f32 v[66:67], v[30:31], v[62:63], v[62:63]
	v_pk_fma_f32 v[28:29], v[56:57], v[64:65], 1.0 op_sel_hi:[1,1,0] neg_lo:[1,0,0] neg_hi:[1,0,0]
	v_pk_fma_f32 v[30:31], v[58:59], v[66:67], 1.0 op_sel_hi:[1,1,0] neg_lo:[1,0,0] neg_hi:[1,0,0]
	v_pk_fma_f32 v[28:29], v[28:29], v[60:61], v[64:65]
	v_pk_fma_f32 v[30:31], v[30:31], v[62:63], v[66:67]
	v_div_fixup_f32 v28, v28, v56, 1.0
	v_div_fixup_f32 v29, v29, v57, 1.0
	v_div_fixup_f32 v30, v30, v58, 1.0
	v_div_fixup_f32 v31, v31, v59, 1.0
	v_pk_mul_f32 v[10:11], v[10:11], v[28:29]
	v_pk_mul_f32 v[12:13], v[12:13], v[30:31]
	v_lshlrev_b32_e32 v56, 16, v46
	v_and_b32_e32 v57, 0xffff0000, v46
	v_lshlrev_b32_e32 v58, 16, v47
	v_and_b32_e32 v59, 0xffff0000, v47
	v_pk_mul_f32 v[56:57], v[56:57], s[98:99] op_sel_hi:[1,0]
	v_pk_mul_f32 v[58:59], v[58:59], s[98:99] op_sel_hi:[1,0]
	v_exp_f32_e32 v56, v56
	v_exp_f32_e32 v57, v57
	v_exp_f32_e32 v58, v58
	v_exp_f32_e32 v59, v59
	v_pk_add_f32 v[56:57], v[56:57], 1.0 op_sel_hi:[1,0]
	v_pk_add_f32 v[58:59], v[58:59], 1.0 op_sel_hi:[1,0]
	v_rcp_f32_e32 v60, v56
	v_rcp_f32_e32 v61, v57
	v_rcp_f32_e32 v62, v58
	v_rcp_f32_e32 v63, v59
	v_pk_fma_f32 v[28:29], v[56:57], v[60:61], 1.0 op_sel_hi:[1,1,0] neg_lo:[1,0,0] neg_hi:[1,0,0]
	v_pk_fma_f32 v[30:31], v[58:59], v[62:63], 1.0 op_sel_hi:[1,1,0] neg_lo:[1,0,0] neg_hi:[1,0,0]
	v_pk_fma_f32 v[60:61], v[28:29], v[60:61], v[60:61]
	v_pk_fma_f32 v[62:63], v[30:31], v[62:63], v[62:63]
	v_pk_fma_f32 v[28:29], v[56:57], v[60:61], 1.0 op_sel_hi:[1,1,0] neg_lo:[1,0,0] neg_hi:[1,0,0]
	v_pk_fma_f32 v[30:31], v[58:59], v[62:63], 1.0 op_sel_hi:[1,1,0] neg_lo:[1,0,0] neg_hi:[1,0,0]
	v_pk_fma_f32 v[64:65], v[28:29], v[60:61], v[60:61]
	v_pk_fma_f32 v[66:67], v[30:31], v[62:63], v[62:63]
	v_pk_fma_f32 v[28:29], v[56:57], v[64:65], 1.0 op_sel_hi:[1,1,0] neg_lo:[1,0,0] neg_hi:[1,0,0]
	v_pk_fma_f32 v[30:31], v[58:59], v[66:67], 1.0 op_sel_hi:[1,1,0] neg_lo:[1,0,0] neg_hi:[1,0,0]
	v_pk_fma_f32 v[28:29], v[28:29], v[60:61], v[64:65]
	v_pk_fma_f32 v[30:31], v[30:31], v[62:63], v[66:67]
	v_div_fixup_f32 v28, v28, v56, 1.0
	v_div_fixup_f32 v29, v29, v57, 1.0
	v_div_fixup_f32 v30, v30, v58, 1.0
	v_div_fixup_f32 v31, v31, v59, 1.0
	v_pk_mul_f32 v[14:15], v[14:15], v[28:29]
	v_pk_mul_f32 v[16:17], v[16:17], v[30:31]
	v_pk_mul_f32 v[10:11], v[10:11], s[100:101] op_sel_hi:[1,0]
	v_pk_mul_f32 v[12:13], v[12:13], s[100:101] op_sel_hi:[1,0]
	v_pk_mul_f32 v[14:15], v[14:15], s[100:101] op_sel_hi:[1,0]
	v_pk_mul_f32 v[16:17], v[16:17], s[100:101] op_sel_hi:[1,0]
	v_med3_f32 v10, v10, s86, v202
	v_med3_f32 v11, v11, s86, v202
	v_med3_f32 v12, v12, s86, v202
	v_med3_f32 v13, v13, s86, v202
	v_med3_f32 v14, v14, s86, v202
	v_med3_f32 v15, v15, s86, v202
	v_med3_f32 v16, v16, s86, v202
	v_med3_f32 v17, v17, s86, v202
	v_add_u32_e32 v20, 32, v6
	v_mov_b32_e32 v21, 0
	v_cvt_pk_fp8_f32 v26, v10, v11
	v_cvt_pk_fp8_f32 v27, v14, v15
	v_lshlrev_b64 v[20:21], 10, v[20:21]
	v_cvt_pk_fp8_f32 v26, v12, v13 op_sel:[0,0,1]
	v_cvt_pk_fp8_f32 v27, v16, v17 op_sel:[0,0,1]
	v_lshl_add_u64 v[20:21], v[4:5], 0, v[20:21]
	s_nop 0
	global_store_dwordx2 v[20:21], v[26:27], off
	v_add_u32_e32 v9, 64, v6
	v_lshl_add_u32 v7, v9, 8, v8
	ds_read_b128 v[22:25], v7
	s_waitcnt vmcnt(3) lgkmcnt(0)
; #define LAS __attribute__((address_space(3)))
; __device__ __forceinline__ float sigmoidf_(float x) { return 1.f / (1.f + __expf(-x)); }
; __device__ __forceinline__ unsigned pk4_fp8c(float a, float b, float c, float d) { return pk4_fp8(__builtin_amdgcn_fmed3f(a, -448.f, 448.f), __builtin_amdgcn_fmed3f(b, -448.f, 448.f), __builtin_amdgcn_fmed3f(c, -448.f, 448.f), __builtin_amdgcn_fmed3f(d, -448.f, 448.f)); }
; __device__ __forceinline__ void out_unit_m(LAS unsigned char* lds, LAS unsigned char* ldstab, const OutArgs a, const int wv) {
;     ...
;     for (int id = tid; id < 128 * 16; id += 512) { const int row = id >> 4, ch = id & 15;
;         const u32x4 y = *(const LAS u32x4*)(lds + row * TP + ch * 16); const u32x4 g = *(const u32x4*)(a.G + (size_t)row * a.ldg + 8 * ch);
;         const f32x4 g0 = *(const f32x4*)(a.gain + 8 * ch), g1 = *(const f32x4*)(a.gain + 8 * ch + 4);
;         const float yv[8] = {bf_lo(y.x), bf_hi(y.x), bf_lo(y.y), bf_hi(y.y), bf_lo(y.z), bf_hi(y.z), bf_lo(y.w), bf_hi(y.w)};
;         const float gv[8] = {bf_lo(g.x), bf_hi(g.x), bf_lo(g.y), bf_hi(g.y), bf_lo(g.z), bf_hi(g.z), bf_lo(g.w), bf_hi(g.w)};
;         const float gn[8] = {g0[0], g0[1], g0[2], g0[3], g1[0], g1[1], g1[2], g1[3]};
;         float ov[8];
; #pragma unroll
;         for (int i = 0; i < 8; ++i) ov[i] = yv[i] * gn[i] * sigmoidf_(gv[i]);
;         u32x2 w; w.x = pg8::pk4_fp8c(ov[0] * a.oscale, ov[1] * a.oscale, ov[2] * a.oscale, ov[3] * a.oscale); w.y = pg8::pk4_fp8c(ov[4] * a.oscale, ov[5] * a.oscale, ov[6] * a.oscale, ov[7] * a.oscale);
;         *(u32x2*)(a.Out + (size_t)row * a.ldo + 8 * ch) = w; }
	v_lshlrev_b32_e32 v10, 16, v22
	v_and_b32_e32 v11, 0xffff0000, v22
	v_lshlrev_b32_e32 v12, 16, v23
	v_and_b32_e32 v13, 0xffff0000, v23
	v_lshlrev_b32_e32 v14, 16, v24
	v_and_b32_e32 v15, 0xffff0000, v24
	v_lshlrev_b32_e32 v16, 16, v25
	v_and_b32_e32 v17, 0xffff0000, v25
	v_pk_mul_f32 v[10:11], v[32:33], v[10:11]
	v_pk_mul_f32 v[12:13], v[34:35], v[12:13]
	v_pk_mul_f32 v[14:15], v[36:37], v[14:15]
	v_pk_mul_f32 v[16:17], v[38:39], v[16:17]
	v_lshlrev_b32_e32 v56, 16, v48
	v_and_b32_e32 v57, 0xffff0000, v48
	v_lshlrev_b32_e32 v58, 16, v49
	v_and_b32_e32 v59, 0xffff0000, v49
	v_pk_mul_f32 v[56:57], v[56:57], s[98:99] op_sel_hi:[1,0]
	v_pk_mul_f32 v[58:59], v[58:59], s[98:99] op_sel_hi:[1,0]
	v_exp_f32_e32 v56, v56
	v_exp_f32_e32 v57, v57
	v_exp_f32_e32 v58, v58
	v_exp_f32_e32 v59, v59
	v_pk_add_f32 v[56:57], v[56:57], 1.0 op_sel_hi:[1,0]
	v_pk_add_f32 v[58:59], v[58:59], 1.0 op_sel_hi:[1,0]
	v_rcp_f32_e32 v60, v56
	v_rcp_f32_e32 v61, v57
	v_rcp_f32_e32 v62, v58
	v_rcp_f32_e32 v63, v59
	v_pk_fma_f32 v[28:29], v[56:57], v[60:61], 1.0 op_sel_hi:[1,1,0] neg_lo:[1,0,0] neg_hi:[1,0,0]
	v_pk_fma_f32 v[30:31], v[58:59], v[62:63], 1.0 op_sel_hi:[1,1,0] neg_lo:[1,0,0] neg_hi:[1,0,0]
	v_pk_fma_f32 v[60:61], v[28:29], v[60:61], v[60:61]
	v_pk_fma_f32 v[62:63], v[30:31], v[62:63], v[62:63]
	v_pk_fma_f32 v[28:29], v[56:57], v[60:61], 1.0 op_sel_hi:[1,1,0] neg_lo:[1,0,0] neg_hi:[1,0,0]
	v_pk_fma_f32 v[30:31], v[58:59], v[62:63], 1.0 op_sel_hi:[1,1,0] neg_lo:[1,0,0] neg_hi:[1,0,0]
	v_pk_fma_f32 v[64:65], v[28:29], v[60:61], v[60:61]
	v_pk_fma_f32 v[66:67], v[30:31], v[62:63], v[62:63]
	v_pk_fma_f32 v[28:29], v[56:57], v[64:65], 1.0 op_sel_hi:[1,1,0] neg_lo:[1,0,0] neg_hi:[1,0,0]
	v_pk_fma_f32 v[30:31], v[58:59], v[66:67], 1.0 op_sel_hi:[1,1,0] neg_lo:[1,0,0] neg_hi:[1,0,0]
	v_pk_fma_f32 v[28:29], v[28:29], v[60:61], v[64:65]
	v_pk_fma_f32 v[30:31], v[30:31], v[62:63], v[66:67]
	v_div_fixup_f32 v28, v28, v56, 1.0
	v_div_fixup_f32 v29, v29, v57, 1.0
	v_div_fixup_f32 v30, v30, v58, 1.0
	v_div_fixup_f32 v31, v31, v59, 1.0
	v_pk_mul_f32 v[10:11], v[10:11], v[28:29]
	v_pk_mul_f32 v[12:13], v[12:13], v[30:31]
	v_lshlrev_b32_e32 v56, 16, v50
	v_and_b32_e32 v57, 0xffff0000, v50
	v_lshlrev_b32_e32 v58, 16, v51
	v_and_b32_e32 v59, 0xffff0000, v51
	v_pk_mul_f32 v[56:57], v[56:57], s[98:99] op_sel_hi:[1,0]
	v_pk_mul_f32 v[58:59], v[58:59], s[98:99] op_sel_hi:[1,0]
	v_exp_f32_e32 v56, v56
	v_exp_f32_e32 v57, v57
	v_exp_f32_e32 v58, v58
	v_exp_f32_e32 v59, v59
	v_pk_add_f32 v[56:57], v[56:57], 1.0 op_sel_hi:[1,0]
	v_pk_add_f32 v[58:59], v[58:59], 1.0 op_sel_hi:[1,0]
	v_rcp_f32_e32 v60, v56
	v_rcp_f32_e32 v61, v57
	v_rcp_f32_e32 v62, v58
	v_rcp_f32_e32 v63, v59
	v_pk_fma_f32 v[28:29], v[56:57], v[60:61], 1.0 op_sel_hi:[1,1,0] neg_lo:[1,0,0] neg_hi:[1,0,0]
	v_pk_fma_f32 v[30:31], v[58:59], v[62:63], 1.0 op_sel_hi:[1,1,0] neg_lo:[1,0,0] neg_hi:[1,0,0]
	v_pk_fma_f32 v[60:61], v[28:29], v[60:61], v[60:61]
	v_pk_fma_f32 v[62:63], v[30:31], v[62:63], v[62:63]
	v_pk_fma_f32 v[28:29], v[56:57], v[60:61], 1.0 op_sel_hi:[1,1,0] neg_lo:[1,0,0] neg_hi:[1,0,0]
	v_pk_fma_f32 v[30:31], v[58:59], v[62:63], 1.0 op_sel_hi:[1,1,0] neg_lo:[1,0,0] neg_hi:[1,0,0]
	v_pk_fma_f32 v[64:65], v[28:29], v[60:61], v[60:61]
	v_pk_fma_f32 v[66:67], v[30:31], v[62:63], v[62:63]
	v_pk_fma_f32 v[28:29], v[56:57], v[64:65], 1.0 op_sel_hi:[1,1,0] neg_lo:[1,0,0] neg_hi:[1,0,0]
	v_pk_fma_f32 v[30:31], v[58:59], v[66:67], 1.0 op_sel_hi:[1,1,0] neg_lo:[1,0,0] neg_hi:[1,0,0]
	v_pk_fma_f32 v[28:29], v[28:29], v[60:61], v[64:65]
	v_pk_fma_f32 v[30:31], v[30:31], v[62:63], v[66:67]
	v_div_fixup_f32 v28, v28, v56, 1.0
	v_div_fixup_f32 v29, v29, v57, 1.0
	v_div_fixup_f32 v30, v30, v58, 1.0
	v_div_fixup_f32 v31, v31, v59, 1.0
	v_pk_mul_f32 v[14:15], v[14:15], v[28:29]
	v_pk_mul_f32 v[16:17], v[16:17], v[30:31]
	v_pk_mul_f32 v[10:11], v[10:11], s[100:101] op_sel_hi:[1,0]
	v_pk_mul_f32 v[12:13], v[12:13], s[100:101] op_sel_hi:[1,0]
	v_pk_mul_f32 v[14:15], v[14:15], s[100:101] op_sel_hi:[1,0]
	v_pk_mul_f32 v[16:17], v[16:17], s[100:101] op_sel_hi:[1,0]
	v_med3_f32 v10, v10, s86, v202
	v_med3_f32 v11, v11, s86, v202
	v_med3_f32 v12, v12, s86, v202
	v_med3_f32 v13, v13, s86, v202
	v_med3_f32 v14, v14, s86, v202
	v_med3_f32 v15, v15, s86, v202
	v_med3_f32 v16, v16, s86, v202
	v_med3_f32 v17, v17, s86, v202
	v_add_u32_e32 v20, 64, v6
	v_mov_b32_e32 v21, 0
	v_cvt_pk_fp8_f32 v26, v10, v11
	v_cvt_pk_fp8_f32 v27, v14, v15
	v_lshlrev_b64 v[20:21], 10, v[20:21]
	v_cvt_pk_fp8_f32 v26, v12, v13 op_sel:[0,0,1]
	v_cvt_pk_fp8_f32 v27, v16, v17 op_sel:[0,0,1]
	v_lshl_add_u64 v[20:21], v[4:5], 0, v[20:21]
	s_nop 0
	global_store_dwordx2 v[20:21], v[26:27], off
	v_add_u32_e32 v9, 96, v6
	v_lshl_add_u32 v7, v9, 8, v8
	ds_read_b128 v[22:25], v7
	s_waitcnt vmcnt(3) lgkmcnt(0)
; #define LAS __attribute__((address_space(3)))
; __device__ __forceinline__ float sigmoidf_(float x) { return 1.f / (1.f + __expf(-x)); }
; __device__ __forceinline__ unsigned pk4_fp8c(float a, float b, float c, float d) { return pk4_fp8(__builtin_amdgcn_fmed3f(a, -448.f, 448.f), __builtin_amdgcn_fmed3f(b, -448.f, 448.f), __builtin_amdgcn_fmed3f(c, -448.f, 448.f), __builtin_amdgcn_fmed3f(d, -448.f, 448.f)); }
; __device__ __forceinline__ void out_unit_m(LAS unsigned char* lds, LAS unsigned char* ldstab, const OutArgs a, const int wv) {
;     ...
;     for (int id = tid; id < 128 * 16; id += 512) { const int row = id >> 4, ch = id & 15;
;         const u32x4 y = *(const LAS u32x4*)(lds + row * TP + ch * 16); const u32x4 g = *(const u32x4*)(a.G + (size_t)row * a.ldg + 8 * ch);
;         const f32x4 g0 = *(const f32x4*)(a.gain + 8 * ch), g1 = *(const f32x4*)(a.gain + 8 * ch + 4);
;         const float yv[8] = {bf_lo(y.x), bf_hi(y.x), bf_lo(y.y), bf_hi(y.y), bf_lo(y.z), bf_hi(y.z), bf_lo(y.w), bf_hi(y.w)};
;         const float gv[8] = {bf_lo(g.x), bf_hi(g.x), bf_lo(g.y), bf_hi(g.y), bf_lo(g.z), bf_hi(g.z), bf_lo(g.w), bf_hi(g.w)};
;         const float gn[8] = {g0[0], g0[1], g0[2], g0[3], g1[0], g1[1], g1[2], g1[3]};
;         float ov[8];
; #pragma unroll
;         for (int i = 0; i < 8; ++i) ov[i] = yv[i] * gn[i] * sigmoidf_(gv[i]);
;         u32x2 w; w.x = pg8::pk4_fp8c(ov[0] * a.oscale, ov[1] * a.oscale, ov[2] * a.oscale, ov[3] * a.oscale); w.y = pg8::pk4_fp8c(ov[4] * a.oscale, ov[5] * a.oscale, ov[6] * a.oscale, ov[7] * a.oscale);
;         *(u32x2*)(a.Out + (size_t)row * a.ldo + 8 * ch) = w; }
	v_lshlrev_b32_e32 v10, 16, v22
	v_and_b32_e32 v11, 0xffff0000, v22
	v_lshlrev_b32_e32 v12, 16, v23
	v_and_b32_e32 v13, 0xffff0000, v23
	v_lshlrev_b32_e32 v14, 16, v24
	v_and_b32_e32 v15, 0xffff0000, v24
	v_lshlrev_b32_e32 v16, 16, v25
	v_and_b32_e32 v17, 0xffff0000, v25
	v_pk_mul_f32 v[10:11], v[32:33], v[10:11]
	v_pk_mul_f32 v[12:13], v[34:35], v[12:13]
	v_pk_mul_f32 v[14:15], v[36:37], v[14:15]
	v_pk_mul_f32 v[16:17], v[38:39], v[16:17]
	v_lshlrev_b32_e32 v56, 16, v52
	v_and_b32_e32 v57, 0xffff0000, v52
	v_lshlrev_b32_e32 v58, 16, v53
	v_and_b32_e32 v59, 0xffff0000, v53
	v_pk_mul_f32 v[56:57], v[56:57], s[98:99] op_sel_hi:[1,0]
	v_pk_mul_f32 v[58:59], v[58:59], s[98:99] op_sel_hi:[1,0]
	v_exp_f32_e32 v56, v56
	v_exp_f32_e32 v57, v57
	v_exp_f32_e32 v58, v58
	v_exp_f32_e32 v59, v59
	v_pk_add_f32 v[56:57], v[56:57], 1.0 op_sel_hi:[1,0]
	v_pk_add_f32 v[58:59], v[58:59], 1.0 op_sel_hi:[1,0]
	v_rcp_f32_e32 v60, v56
	v_rcp_f32_e32 v61, v57
	v_rcp_f32_e32 v62, v58
	v_rcp_f32_e32 v63, v59
	v_pk_fma_f32 v[28:29], v[56:57], v[60:61], 1.0 op_sel_hi:[1,1,0] neg_lo:[1,0,0] neg_hi:[1,0,0]
	v_pk_fma_f32 v[30:31], v[58:59], v[62:63], 1.0 op_sel_hi:[1,1,0] neg_lo:[1,0,0] neg_hi:[1,0,0]
	v_pk_fma_f32 v[60:61], v[28:29], v[60:61], v[60:61]
	v_pk_fma_f32 v[62:63], v[30:31], v[62:63], v[62:63]
	v_pk_fma_f32 v[28:29], v[56:57], v[60:61], 1.0 op_sel_hi:[1,1,0] neg_lo:[1,0,0] neg_hi:[1,0,0]
	v_pk_fma_f32 v[30:31], v[58:59], v[62:63], 1.0 op_sel_hi:[1,1,0] neg_lo:[1,0,0] neg_hi:[1,0,0]
	v_pk_fma_f32 v[64:65], v[28:29], v[60:61], v[60:61]
	v_pk_fma_f32 v[66:67], v[30:31], v[62:63], v[62:63]
	v_pk_fma_f32 v[28:29], v[56:57], v[64:65], 1.0 op_sel_hi:[1,1,0] neg_lo:[1,0,0] neg_hi:[1,0,0]
	v_pk_fma_f32 v[30:31], v[58:59], v[66:67], 1.0 op_sel_hi:[1,1,0] neg_lo:[1,0,0] neg_hi:[1,0,0]
	v_pk_fma_f32 v[28:29], v[28:29], v[60:61], v[64:65]
	v_pk_fma_f32 v[30:31], v[30:31], v[62:63], v[66:67]
	v_div_fixup_f32 v28, v28, v56, 1.0
	v_div_fixup_f32 v29, v29, v57, 1.0
	v_div_fixup_f32 v30, v30, v58, 1.0
	v_div_fixup_f32 v31, v31, v59, 1.0
	v_pk_mul_f32 v[10:11], v[10:11], v[28:29]
	v_pk_mul_f32 v[12:13], v[12:13], v[30:31]
	v_lshlrev_b32_e32 v56, 16, v54
	v_and_b32_e32 v57, 0xffff0000, v54
	v_lshlrev_b32_e32 v58, 16, v55
	v_and_b32_e32 v59, 0xffff0000, v55
	v_pk_mul_f32 v[56:57], v[56:57], s[98:99] op_sel_hi:[1,0]
	v_pk_mul_f32 v[58:59], v[58:59], s[98:99] op_sel_hi:[1,0]
	v_exp_f32_e32 v56, v56
	v_exp_f32_e32 v57, v57
	v_exp_f32_e32 v58, v58
	v_exp_f32_e32 v59, v59
	v_pk_add_f32 v[56:57], v[56:57], 1.0 op_sel_hi:[1,0]
	v_pk_add_f32 v[58:59], v[58:59], 1.0 op_sel_hi:[1,0]
	v_rcp_f32_e32 v60, v56
	v_rcp_f32_e32 v61, v57
	v_rcp_f32_e32 v62, v58
	v_rcp_f32_e32 v63, v59
	v_pk_fma_f32 v[28:29], v[56:57], v[60:61], 1.0 op_sel_hi:[1,1,0] neg_lo:[1,0,0] neg_hi:[1,0,0]
	v_pk_fma_f32 v[30:31], v[58:59], v[62:63], 1.0 op_sel_hi:[1,1,0] neg_lo:[1,0,0] neg_hi:[1,0,0]
	v_pk_fma_f32 v[60:61], v[28:29], v[60:61], v[60:61]
	v_pk_fma_f32 v[62:63], v[30:31], v[62:63], v[62:63]
	v_pk_fma_f32 v[28:29], v[56:57], v[60:61], 1.0 op_sel_hi:[1,1,0] neg_lo:[1,0,0] neg_hi:[1,0,0]
	v_pk_fma_f32 v[30:31], v[58:59], v[62:63], 1.0 op_sel_hi:[1,1,0] neg_lo:[1,0,0] neg_hi:[1,0,0]
	v_pk_fma_f32 v[64:65], v[28:29], v[60:61], v[60:61]
	v_pk_fma_f32 v[66:67], v[30:31], v[62:63], v[62:63]
	v_pk_fma_f32 v[28:29], v[56:57], v[64:65], 1.0 op_sel_hi:[1,1,0] neg_lo:[1,0,0] neg_hi:[1,0,0]
	v_pk_fma_f32 v[30:31], v[58:59], v[66:67], 1.0 op_sel_hi:[1,1,0] neg_lo:[1,0,0] neg_hi:[1,0,0]
	v_pk_fma_f32 v[28:29], v[28:29], v[60:61], v[64:65]
	v_pk_fma_f32 v[30:31], v[30:31], v[62:63], v[66:67]
	v_div_fixup_f32 v28, v28, v56, 1.0
	v_div_fixup_f32 v29, v29, v57, 1.0
	v_div_fixup_f32 v30, v30, v58, 1.0
	v_div_fixup_f32 v31, v31, v59, 1.0
	v_pk_mul_f32 v[14:15], v[14:15], v[28:29]
	v_pk_mul_f32 v[16:17], v[16:17], v[30:31]
	v_pk_mul_f32 v[10:11], v[10:11], s[100:101] op_sel_hi:[1,0]
	v_pk_mul_f32 v[12:13], v[12:13], s[100:101] op_sel_hi:[1,0]
	v_pk_mul_f32 v[14:15], v[14:15], s[100:101] op_sel_hi:[1,0]
	v_pk_mul_f32 v[16:17], v[16:17], s[100:101] op_sel_hi:[1,0]
	v_med3_f32 v10, v10, s86, v202
	v_med3_f32 v11, v11, s86, v202
	v_med3_f32 v12, v12, s86, v202
	v_med3_f32 v13, v13, s86, v202
	v_med3_f32 v14, v14, s86, v202
	v_med3_f32 v15, v15, s86, v202
	v_med3_f32 v16, v16, s86, v202
	v_med3_f32 v17, v17, s86, v202
	v_add_u32_e32 v20, 96, v6
	v_mov_b32_e32 v21, 0
	v_cvt_pk_fp8_f32 v26, v10, v11
	v_cvt_pk_fp8_f32 v27, v14, v15
	v_lshlrev_b64 v[20:21], 10, v[20:21]
	v_cvt_pk_fp8_f32 v26, v12, v13 op_sel:[0,0,1]
	v_cvt_pk_fp8_f32 v27, v16, v17 op_sel:[0,0,1]
	v_lshl_add_u64 v[20:21], v[4:5], 0, v[20:21]
	s_nop 0
	global_store_dwordx2 v[20:21], v[26:27], off

; #define LAS __attribute__((address_space(3)))
; __device__ __forceinline__ bf16_t f2bf(float f) { unsigned u = __builtin_bit_cast(unsigned, f); return (bf16_t)((u + 0x7fffu + ((u >> 16) & 1u)) >> 16); }
; __device__ __forceinline__ int crow(int r, int hi) { return (r & 3) + 8 * (r >> 2) + 4 * hi; }
; __device__ __forceinline__ int crow(int r, int hi) { return (r & 3) + 8 * (r >> 2) + 4 * hi; }
; __device__ __forceinline__ void out_unit_m(LAS unsigned char* lds, LAS unsigned char* ldstab, const OutArgs a, const int wv) {
;     ...
;     __syncthreads();
;     constexpr int TP = DV * 2;
; #pragma unroll
;     for (int r = 0; r < 16; ++r) { const int row = 32 * rb + crow(r, hi);
;         const float inv = rsqrtf((s2[r] + exch[(1 - dh) * 128 + row]) * (1.f / DV) + EPS);
; #pragma unroll
;         for (int nb = 0; nb < 2; ++nb) *(LAS bf16_t*)(lds + row * TP + (dh * 64 + 32 * nb + r32) * 2) = f2bf(o[nb][r] * inv); }
.LBB0_3189:
	s_or_b64 exec, exec, s[6:7]
	v_or_b32_e32 v56, s12, v156
	s_lshl_b32 s6, s8, 7
	v_subrev_u32_e32 v48, s6, v56
	s_add_i32 s7, 0, 0x22100
	v_lshl_add_u32 v48, v48, 2, s7
	s_waitcnt lgkmcnt(0)
	s_barrier
	ds_read_b128 v[48:51], v48 offset:512
	v_or_b32_e32 v57, 8, v56
	v_subrev_u32_e32 v52, s6, v57
	v_lshl_add_u32 v52, v52, 2, s7
	ds_read_b128 v[52:55], v52 offset:512
	s_waitcnt lgkmcnt(1)
	v_pk_add_f32 v[48:49], v[44:45], v[48:49]
	v_mov_b64_e32 v[44:45], s[46:47]
	v_pk_fma_f32 v[48:49], v[48:49], s[44:45], v[44:45] op_sel_hi:[1,0,0]
	v_lshlrev_b32_e32 v59, 1, v159
	v_mul_f32_e32 v58, 0x4b800000, v48
	v_cmp_gt_f32_e32 vcc, s83, v48
	s_add_i32 s8, s6, 0
	s_nop 0
	v_cndmask_b32_e32 v48, v48, v58, vcc
	v_rsq_f32_e32 v48, v48
	v_lshlrev_b32_e32 v58, 8, v56
	v_add3_u32 v58, s8, v58, v59
	v_mul_f32_e32 v60, 0x45800000, v48
	v_cndmask_b32_e32 v48, v48, v60, vcc
	v_mul_f32_e32 v0, v0, v48
	v_bfe_u32 v60, v0, 16, 1
	v_add3_u32 v0, v0, v60, s84
	ds_write_b16_d16_hi v58, v0
	v_mul_f32_e32 v0, v16, v48
	v_mul_f32_e32 v16, 0x4b800000, v49
	v_cmp_gt_f32_e32 vcc, s83, v49
	v_bfe_u32 v48, v0, 16, 1
	v_add3_u32 v0, v0, v48, s84
	v_cndmask_b32_e32 v16, v49, v16, vcc
	v_rsq_f32_e32 v16, v16
	ds_write_b16_d16_hi v58, v0 offset:64
	v_mul_f32_e32 v0, 0x45800000, v16
	v_cndmask_b32_e32 v0, v16, v0, vcc
	v_mul_f32_e32 v1, v1, v0
	v_bfe_u32 v16, v1, 16, 1
	v_add3_u32 v1, v1, v16, s84
	ds_write_b16_d16_hi v58, v1 offset:256
	v_mul_f32_e32 v16, v17, v0
	v_pk_add_f32 v[0:1], v[46:47], v[50:51]
	s_nop 0
	v_pk_fma_f32 v[0:1], v[0:1], s[44:45], v[44:45] op_sel_hi:[1,0,0]
	s_nop 0
	v_mul_f32_e32 v17, 0x4b800000, v0
	v_cmp_gt_f32_e32 vcc, s83, v0
	s_nop 1
	v_cndmask_b32_e32 v0, v0, v17, vcc
	v_rsq_f32_e32 v0, v0
	v_bfe_u32 v17, v16, 16, 1
	v_add3_u32 v16, v16, v17, s84
	ds_write_b16_d16_hi v58, v16 offset:320
	v_mul_f32_e32 v16, 0x45800000, v0
	v_cndmask_b32_e32 v0, v0, v16, vcc
	v_mul_f32_e32 v2, v2, v0
	v_bfe_u32 v16, v2, 16, 1
	v_add3_u32 v2, v2, v16, s84
	ds_write_b16_d16_hi v58, v2 offset:512
	v_mul_f32_e32 v2, 0x4b800000, v1
	v_cmp_gt_f32_e32 vcc, s83, v1
	v_mul_f32_e32 v0, v18, v0
	v_or_b32_e32 v17, 16, v56
	v_cndmask_b32_e32 v1, v1, v2, vcc
	v_rsq_f32_e32 v1, v1
	v_bfe_u32 v2, v0, 16, 1
	v_add3_u32 v0, v0, v2, s84
	ds_write_b16_d16_hi v58, v0 offset:576
	v_mul_f32_e32 v0, 0x45800000, v1
	v_cndmask_b32_e32 v0, v1, v0, vcc
	v_mul_f32_e32 v1, v3, v0
	v_bfe_u32 v2, v1, 16, 1
	v_add3_u32 v1, v1, v2, s84
	v_mul_f32_e32 v0, v19, v0
	ds_write_b16_d16_hi v58, v1 offset:768
	v_bfe_u32 v1, v0, 16, 1
	v_add3_u32 v2, v0, v1, s84
	s_waitcnt lgkmcnt(7)
	v_pk_add_f32 v[0:1], v[40:41], v[52:53]
	ds_write_b16_d16_hi v58, v2 offset:832
	v_pk_fma_f32 v[0:1], v[0:1], s[44:45], v[44:45] op_sel_hi:[1,0,0]
	v_lshlrev_b32_e32 v2, 8, v57
	v_mul_f32_e32 v3, 0x4b800000, v0
	v_cmp_gt_f32_e32 vcc, s83, v0
	v_add3_u32 v2, s8, v2, v59
	v_or_b32_e32 v18, 24, v56
	v_cndmask_b32_e32 v0, v0, v3, vcc
	v_rsq_f32_e32 v0, v0
	s_nop 0
	v_mul_f32_e32 v3, 0x45800000, v0
	v_cndmask_b32_e32 v0, v0, v3, vcc
	v_mul_f32_e32 v3, v4, v0
	v_bfe_u32 v4, v3, 16, 1
	v_add3_u32 v3, v3, v4, s84
	ds_write_b16_d16_hi v2, v3
	v_mul_f32_e32 v3, 0x4b800000, v1
	v_cmp_gt_f32_e32 vcc, s83, v1
	v_mul_f32_e32 v0, v20, v0
	v_subrev_u32_e32 v4, s6, v18
	v_cndmask_b32_e32 v1, v1, v3, vcc
	v_rsq_f32_e32 v1, v1
	v_bfe_u32 v3, v0, 16, 1
	v_add3_u32 v0, v0, v3, s84
	ds_write_b16_d16_hi v2, v0 offset:64
	v_mul_f32_e32 v0, 0x45800000, v1
	v_cndmask_b32_e32 v0, v1, v0, vcc
	v_mul_f32_e32 v1, v5, v0
	v_bfe_u32 v2, v1, 16, 1
	v_add3_u32 v1, v1, v2, s84
	ds_write_b16_d16_hi v58, v1 offset:2304
	v_mul_f32_e32 v2, v21, v0
	v_pk_add_f32 v[0:1], v[42:43], v[54:55]
	v_lshl_add_u32 v4, v4, 2, s7
	v_pk_fma_f32 v[0:1], v[0:1], s[44:45], v[44:45] op_sel_hi:[1,0,0]
	s_nop 0
	v_mul_f32_e32 v3, 0x4b800000, v0
	v_cmp_gt_f32_e32 vcc, s83, v0
	s_nop 1
	v_cndmask_b32_e32 v0, v0, v3, vcc
	v_rsq_f32_e32 v0, v0
	v_bfe_u32 v3, v2, 16, 1
	v_add3_u32 v2, v2, v3, s84
	ds_write_b16_d16_hi v58, v2 offset:2368
	v_mul_f32_e32 v2, 0x45800000, v0
	v_cndmask_b32_e32 v0, v0, v2, vcc
	v_mul_f32_e32 v2, v6, v0
	v_bfe_u32 v3, v2, 16, 1
	v_add3_u32 v2, v2, v3, s84
	ds_write_b16_d16_hi v58, v2 offset:2560
	v_mul_f32_e32 v2, 0x4b800000, v1
	v_cmp_gt_f32_e32 vcc, s83, v1
	v_mul_f32_e32 v0, v22, v0
	s_nop 0
	v_cndmask_b32_e32 v1, v1, v2, vcc
	v_rsq_f32_e32 v1, v1
	v_bfe_u32 v2, v0, 16, 1
	v_add3_u32 v0, v0, v2, s84
	ds_write_b16_d16_hi v58, v0 offset:2624
	v_mul_f32_e32 v0, 0x45800000, v1
	v_cndmask_b32_e32 v0, v1, v0, vcc
	v_mul_f32_e32 v1, v7, v0
	v_bfe_u32 v2, v1, 16, 1
	v_add3_u32 v1, v1, v2, s84
	v_mul_f32_e32 v0, v23, v0
	ds_write_b16_d16_hi v58, v1 offset:2816
	v_bfe_u32 v1, v0, 16, 1
	v_add3_u32 v16, v0, v1, s84
	v_subrev_u32_e32 v0, s6, v17
	v_lshl_add_u32 v0, v0, 2, s7
	ds_read_b128 v[0:3], v0 offset:512
	ds_read_b128 v[4:7], v4 offset:512
	ds_write_b16_d16_hi v58, v16 offset:2880
	v_lshlrev_b32_e32 v16, 8, v17
	v_add3_u32 v16, s8, v16, v59
	s_waitcnt lgkmcnt(2)
; #define LAS __attribute__((address_space(3)))
; __device__ __forceinline__ bf16_t f2bf(float f) { unsigned u = __builtin_bit_cast(unsigned, f); return (bf16_t)((u + 0x7fffu + ((u >> 16) & 1u)) >> 16); }
; __device__ __forceinline__ int crow(int r, int hi) { return (r & 3) + 8 * (r >> 2) + 4 * hi; }
; __device__ __forceinline__ int crow(int r, int hi) { return (r & 3) + 8 * (r >> 2) + 4 * hi; }
; __device__ __forceinline__ void out_unit_m(LAS unsigned char* lds, LAS unsigned char* ldstab, const OutArgs a, const int wv) {
;     ...
;     __syncthreads();
;     constexpr int TP = DV * 2;
; #pragma unroll
;     for (int r = 0; r < 16; ++r) { const int row = 32 * rb + crow(r, hi);
;         const float inv = rsqrtf((s2[r] + exch[(1 - dh) * 128 + row]) * (1.f / DV) + EPS);
; #pragma unroll
;         for (int nb = 0; nb < 2; ++nb) *(LAS bf16_t*)(lds + row * TP + (dh * 64 + 32 * nb + r32) * 2) = f2bf(o[nb][r] * inv); }
;     __syncthreads();
; #pragma unroll 1
;     for (int id = tid; id < 128 * 16; id += 512) { const int row = id >> 4, ch = id & 15;
;         const u32x4 y = *(const LAS u32x4*)(lds + row * TP + ch * 16); const u32x4 g = *(const u32x4*)(a.G + (size_t)row * a.ldg + 8 * ch);
;         const f32x4 g0 = *(const f32x4*)(a.gain + 8 * ch), g1 = *(const f32x4*)(a.gain + 8 * ch + 4);
;         const float yv[8] = {bf_lo(y.x), bf_hi(y.x), bf_lo(y.y), bf_hi(y.y), bf_lo(y.z), bf_hi(y.z), bf_lo(y.w), bf_hi(y.w)};
;         const float gv[8] = {bf_lo(g.x), bf_hi(g.x), bf_lo(g.y), bf_hi(g.y), bf_lo(g.z), bf_hi(g.z), bf_lo(g.w), bf_hi(g.w)};
	v_pk_add_f32 v[0:1], v[36:37], v[0:1]
	s_nop 0
	v_pk_fma_f32 v[0:1], v[0:1], s[44:45], v[44:45] op_sel_hi:[1,0,0]
	s_nop 0
	v_mul_f32_e32 v19, 0x4b800000, v0
	v_cmp_gt_f32_e32 vcc, s83, v0
	s_nop 1
	v_cndmask_b32_e32 v0, v0, v19, vcc
	v_rsq_f32_e32 v0, v0
	s_nop 0
	v_mul_f32_e32 v17, 0x45800000, v0
	v_cndmask_b32_e32 v0, v0, v17, vcc
	v_mul_f32_e32 v8, v8, v0
	v_bfe_u32 v17, v8, 16, 1
	v_add3_u32 v8, v8, v17, s84
	ds_write_b16_d16_hi v16, v8
	v_mul_f32_e32 v8, 0x4b800000, v1
	v_cmp_gt_f32_e32 vcc, s83, v1
	v_mul_f32_e32 v0, v24, v0
	s_nop 0
	v_cndmask_b32_e32 v1, v1, v8, vcc
	v_rsq_f32_e32 v1, v1
	v_bfe_u32 v8, v0, 16, 1
	v_add3_u32 v0, v0, v8, s84
	ds_write_b16_d16_hi v16, v0 offset:64
	v_mul_f32_e32 v0, 0x45800000, v1
	v_cndmask_b32_e32 v0, v1, v0, vcc
	v_mul_f32_e32 v1, v9, v0
	v_bfe_u32 v8, v1, 16, 1
	v_add3_u32 v1, v1, v8, s84
	ds_write_b16_d16_hi v58, v1 offset:4352
	v_mul_f32_e32 v8, v25, v0
	v_pk_add_f32 v[0:1], v[38:39], v[2:3]
	s_nop 0
	v_pk_fma_f32 v[0:1], v[0:1], s[44:45], v[44:45] op_sel_hi:[1,0,0]
	s_nop 0
	v_mul_f32_e32 v2, 0x4b800000, v0
	v_cmp_gt_f32_e32 vcc, s83, v0
	s_nop 1
	v_cndmask_b32_e32 v0, v0, v2, vcc
	v_rsq_f32_e32 v0, v0
	v_bfe_u32 v2, v8, 16, 1
	v_add3_u32 v2, v8, v2, s84
	ds_write_b16_d16_hi v58, v2 offset:4416
	v_mul_f32_e32 v2, 0x45800000, v0
	v_cndmask_b32_e32 v0, v0, v2, vcc
	v_mul_f32_e32 v2, v10, v0
	v_bfe_u32 v3, v2, 16, 1
	v_add3_u32 v2, v2, v3, s84
	ds_write_b16_d16_hi v58, v2 offset:4608
	v_mul_f32_e32 v2, 0x4b800000, v1
	v_cmp_gt_f32_e32 vcc, s83, v1
	v_mul_f32_e32 v0, v26, v0
	s_nop 0
	v_cndmask_b32_e32 v1, v1, v2, vcc
	v_rsq_f32_e32 v1, v1
	v_bfe_u32 v2, v0, 16, 1
	v_add3_u32 v0, v0, v2, s84
	ds_write_b16_d16_hi v58, v0 offset:4672
	v_mul_f32_e32 v0, 0x45800000, v1
	v_cndmask_b32_e32 v0, v1, v0, vcc
	v_mul_f32_e32 v1, v11, v0
	v_bfe_u32 v2, v1, 16, 1
	v_add3_u32 v1, v1, v2, s84
	v_mul_f32_e32 v0, v27, v0
	ds_write_b16_d16_hi v58, v1 offset:4864
	v_bfe_u32 v1, v0, 16, 1
	v_add3_u32 v2, v0, v1, s84
	s_waitcnt lgkmcnt(8)
	v_pk_add_f32 v[0:1], v[32:33], v[4:5]
	ds_write_b16_d16_hi v58, v2 offset:4928
	v_pk_fma_f32 v[0:1], v[0:1], s[44:45], v[44:45] op_sel_hi:[1,0,0]
	v_lshlrev_b32_e32 v2, 8, v18
	v_mul_f32_e32 v3, 0x4b800000, v0
	v_cmp_gt_f32_e32 vcc, s83, v0
	v_add3_u32 v2, s8, v2, v59
	s_nop 0
	v_cndmask_b32_e32 v0, v0, v3, vcc
	v_rsq_f32_e32 v0, v0
	s_nop 0
	v_mul_f32_e32 v3, 0x45800000, v0
	v_cndmask_b32_e32 v0, v0, v3, vcc
	v_mul_f32_e32 v3, v12, v0
	v_bfe_u32 v4, v3, 16, 1
	v_add3_u32 v3, v3, v4, s84
	ds_write_b16_d16_hi v2, v3
	v_mul_f32_e32 v3, 0x4b800000, v1
	v_cmp_gt_f32_e32 vcc, s83, v1
	v_mul_f32_e32 v0, v28, v0
	s_nop 0
	v_cndmask_b32_e32 v1, v1, v3, vcc
	v_rsq_f32_e32 v1, v1
	v_bfe_u32 v3, v0, 16, 1
	v_add3_u32 v0, v0, v3, s84
	ds_write_b16_d16_hi v2, v0 offset:64
	v_mul_f32_e32 v0, 0x45800000, v1
	v_cndmask_b32_e32 v0, v1, v0, vcc
	v_mul_f32_e32 v1, v13, v0
	v_bfe_u32 v2, v1, 16, 1
	v_add3_u32 v1, v1, v2, s84
	ds_write_b16_d16_hi v58, v1 offset:6400
	v_mul_f32_e32 v2, v29, v0
	v_pk_add_f32 v[0:1], v[34:35], v[6:7]
	s_nop 0
	v_pk_fma_f32 v[0:1], v[0:1], s[44:45], v[44:45] op_sel_hi:[1,0,0]
	s_nop 0
	v_mul_f32_e32 v3, 0x4b800000, v0
	v_cmp_gt_f32_e32 vcc, s83, v0
	s_nop 1
	v_cndmask_b32_e32 v0, v0, v3, vcc
	v_rsq_f32_e32 v0, v0
	v_bfe_u32 v3, v2, 16, 1
	v_add3_u32 v2, v2, v3, s84
	ds_write_b16_d16_hi v58, v2 offset:6464
	v_mul_f32_e32 v2, 0x45800000, v0
	v_cndmask_b32_e32 v0, v0, v2, vcc
	v_mul_f32_e32 v2, v14, v0
	v_bfe_u32 v3, v2, 16, 1
	v_add3_u32 v2, v2, v3, s84
	ds_write_b16_d16_hi v58, v2 offset:6656
	v_mul_f32_e32 v2, 0x4b800000, v1
	v_cmp_gt_f32_e32 vcc, s83, v1
	v_mul_f32_e32 v0, v30, v0
	s_nop 0
	v_cndmask_b32_e32 v1, v1, v2, vcc
	v_rsq_f32_e32 v1, v1
	v_bfe_u32 v2, v0, 16, 1
	v_add3_u32 v0, v0, v2, s84
	ds_write_b16_d16_hi v58, v0 offset:6720
	v_mul_f32_e32 v0, 0x45800000, v1
	v_cndmask_b32_e32 v0, v1, v0, vcc
	v_mul_f32_e32 v1, v15, v0
	v_bfe_u32 v2, v1, 16, 1
	v_add3_u32 v1, v1, v2, s84
	v_mul_f32_e32 v0, v31, v0
	ds_write_b16_d16_hi v58, v1 offset:6912
	v_bfe_u32 v1, v0, 16, 1
	v_add3_u32 v0, v0, v1, s84
	v_cmp_gt_i32_e32 vcc, s85, v158
	ds_write_b16_d16_hi v58, v0 offset:6976
	s_waitcnt lgkmcnt(0)
	s_barrier
	s_and_saveexec_b64 s[48:49], vcc
	s_cbranch_execz .LBB0_3192
	s_lshl_b64 s[6:7], s[40:41], 2
	s_add_u32 s4, s4, s6
	s_addc_u32 s5, s5, s7
	s_add_u32 s6, s65, s89
	s_addc_u32 s7, s66, 0
	s_add_u32 s6, s6, s40
	v_and_b32_e32 v2, 15, v158
	s_addc_u32 s7, s7, 0
	v_lshlrev_b32_e32 v0, 4, v2
	v_lshlrev_b32_e32 v156, 3, v2
	v_mov_b32_e32 v1, v157
	v_lshlrev_b32_e32 v2, 5, v2
	v_mov_b32_e32 v3, v157
	v_add_u32_e32 v8, 0, v0
	v_lshl_add_u64 v[0:1], v[160:161], 0, v[0:1]
	v_lshl_add_u64 v[2:3], s[4:5], 0, v[2:3]
	v_lshl_add_u64 v[4:5], s[6:7], 0, v[156:157]
	s_mov_b64 s[50:51], 0
	s_mov_b32 s98, 0xbfb8aa3b
	s_mov_b32 s100, 0x41800000
	v_ashrrev_i32_e32 v6, 4, v158
	global_load_dwordx4 v[36:39], v[2:3], off offset:2064
	global_load_dwordx4 v[32:35], v[2:3], off offset:2048
	v_mad_i64_i32 v[18:19], s[4:5], v6, s71, v[0:1]
	global_load_dwordx4 v[40:43], v[18:19], off offset:3072
	v_add_u32_e32 v9, 32, v6
	v_mad_i64_i32 v[20:21], s[4:5], v9, s71, v[0:1]
	global_load_dwordx4 v[44:47], v[20:21], off offset:3072
	v_add_u32_e32 v9, 64, v6
	v_mad_i64_i32 v[18:19], s[4:5], v9, s71, v[0:1]
	global_load_dwordx4 v[48:51], v[18:19], off offset:3072
	v_add_u32_e32 v9, 96, v6
	v_mad_i64_i32 v[20:21], s[4:5], v9, s71, v[0:1]
	global_load_dwordx4 v[52:55], v[20:21], off offset:3072
	v_lshl_add_u32 v7, v6, 8, v8
	ds_read_b128 v[22:25], v7
	s_waitcnt vmcnt(3) lgkmcnt(0)
; #define LAS __attribute__((address_space(3)))
; __device__ __forceinline__ float sigmoidf_(float x) { return 1.f / (1.f + __expf(-x)); }
; __device__ __forceinline__ unsigned pk4_fp8c(float a, float b, float c, float d) { return pk4_fp8(__builtin_amdgcn_fmed3f(a, -448.f, 448.f), __builtin_amdgcn_fmed3f(b, -448.f, 448.f), __builtin_amdgcn_fmed3f(c, -448.f, 448.f), __builtin_amdgcn_fmed3f(d, -448.f, 448.f)); }
; __device__ __forceinline__ void out_unit_m(LAS unsigned char* lds, LAS unsigned char* ldstab, const OutArgs a, const int wv) {
;     ...
;     for (int id = tid; id < 128 * 16; id += 512) { const int row = id >> 4, ch = id & 15;
;         const u32x4 y = *(const LAS u32x4*)(lds + row * TP + ch * 16); const u32x4 g = *(const u32x4*)(a.G + (size_t)row * a.ldg + 8 * ch);
;         const f32x4 g0 = *(const f32x4*)(a.gain + 8 * ch), g1 = *(const f32x4*)(a.gain + 8 * ch + 4);
;         const float yv[8] = {bf_lo(y.x), bf_hi(y.x), bf_lo(y.y), bf_hi(y.y), bf_lo(y.z), bf_hi(y.z), bf_lo(y.w), bf_hi(y.w)};
;         const float gv[8] = {bf_lo(g.x), bf_hi(g.x), bf_lo(g.y), bf_hi(g.y), bf_lo(g.z), bf_hi(g.z), bf_lo(g.w), bf_hi(g.w)};
;         const float gn[8] = {g0[0], g0[1], g0[2], g0[3], g1[0], g1[1], g1[2], g1[3]};
;         float ov[8];
; #pragma unroll
;         for (int i = 0; i < 8; ++i) ov[i] = yv[i] * gn[i] * sigmoidf_(gv[i]);
;         u32x2 w; w.x = pg8::pk4_fp8c(ov[0] * a.oscale, ov[1] * a.oscale, ov[2] * a.oscale, ov[3] * a.oscale); w.y = pg8::pk4_fp8c(ov[4] * a.oscale, ov[5] * a.oscale, ov[6] * a.oscale, ov[7] * a.oscale);
;         *(u32x2*)(a.Out + (size_t)row * a.ldo + 8 * ch) = w; }
	v_lshlrev_b32_e32 v10, 16, v22
	v_and_b32_e32 v11, 0xffff0000, v22
	v_lshlrev_b32_e32 v12, 16, v23
	v_and_b32_e32 v13, 0xffff0000, v23
	v_lshlrev_b32_e32 v14, 16, v24
	v_and_b32_e32 v15, 0xffff0000, v24
	v_lshlrev_b32_e32 v16, 16, v25
	v_and_b32_e32 v17, 0xffff0000, v25
	v_pk_mul_f32 v[10:11], v[32:33], v[10:11]
	v_pk_mul_f32 v[12:13], v[34:35], v[12:13]
	v_pk_mul_f32 v[14:15], v[36:37], v[14:15]
	v_pk_mul_f32 v[16:17], v[38:39], v[16:17]
	v_lshlrev_b32_e32 v56, 16, v40
	v_and_b32_e32 v57, 0xffff0000, v40
	v_lshlrev_b32_e32 v58, 16, v41
	v_and_b32_e32 v59, 0xffff0000, v41
	v_pk_mul_f32 v[56:57], v[56:57], s[98:99] op_sel_hi:[1,0]
	v_pk_mul_f32 v[58:59], v[58:59], s[98:99] op_sel_hi:[1,0]
	v_exp_f32_e32 v56, v56
	v_exp_f32_e32 v57, v57
	v_exp_f32_e32 v58, v58
	v_exp_f32_e32 v59, v59
	v_pk_add_f32 v[56:57], v[56:57], 1.0 op_sel_hi:[1,0]
	v_pk_add_f32 v[58:59], v[58:59], 1.0 op_sel_hi:[1,0]
	v_rcp_f32_e32 v60, v56
	v_rcp_f32_e32 v61, v57
	v_rcp_f32_e32 v62, v58
	v_rcp_f32_e32 v63, v59
	v_pk_fma_f32 v[28:29], v[56:57], v[60:61], 1.0 op_sel_hi:[1,1,0] neg_lo:[1,0,0] neg_hi:[1,0,0]
	v_pk_fma_f32 v[30:31], v[58:59], v[62:63], 1.0 op_sel_hi:[1,1,0] neg_lo:[1,0,0] neg_hi:[1,0,0]
	v_pk_fma_f32 v[60:61], v[28:29], v[60:61], v[60:61]
	v_pk_fma_f32 v[62:63], v[30:31], v[62:63], v[62:63]
	v_pk_fma_f32 v[28:29], v[56:57], v[60:61], 1.0 op_sel_hi:[1,1,0] neg_lo:[1,0,0] neg_hi:[1,0,0]
	v_pk_fma_f32 v[30:31], v[58:59], v[62:63], 1.0 op_sel_hi:[1,1,0] neg_lo:[1,0,0] neg_hi:[1,0,0]
	v_pk_fma_f32 v[64:65], v[28:29], v[60:61], v[60:61]
	v_pk_fma_f32 v[66:67], v[30:31], v[62:63], v[62:63]
	v_pk_fma_f32 v[28:29], v[56:57], v[64:65], 1.0 op_sel_hi:[1,1,0] neg_lo:[1,0,0] neg_hi:[1,0,0]
	v_pk_fma_f32 v[30:31], v[58:59], v[66:67], 1.0 op_sel_hi:[1,1,0] neg_lo:[1,0,0] neg_hi:[1,0,0]
	v_pk_fma_f32 v[28:29], v[28:29], v[60:61], v[64:65]
	v_pk_fma_f32 v[30:31], v[30:31], v[62:63], v[66:67]
	v_div_fixup_f32 v28, v28, v56, 1.0
	v_div_fixup_f32 v29, v29, v57, 1.0
	v_div_fixup_f32 v30, v30, v58, 1.0
	v_div_fixup_f32 v31, v31, v59, 1.0
	v_pk_mul_f32 v[10:11], v[10:11], v[28:29]
	v_pk_mul_f32 v[12:13], v[12:13], v[30:31]
	v_lshlrev_b32_e32 v56, 16, v42
	v_and_b32_e32 v57, 0xffff0000, v42
	v_lshlrev_b32_e32 v58, 16, v43
	v_and_b32_e32 v59, 0xffff0000, v43
	v_pk_mul_f32 v[56:57], v[56:57], s[98:99] op_sel_hi:[1,0]
	v_pk_mul_f32 v[58:59], v[58:59], s[98:99] op_sel_hi:[1,0]
	v_exp_f32_e32 v56, v56
	v_exp_f32_e32 v57, v57
	v_exp_f32_e32 v58, v58
	v_exp_f32_e32 v59, v59
	v_pk_add_f32 v[56:57], v[56:57], 1.0 op_sel_hi:[1,0]
	v_pk_add_f32 v[58:59], v[58:59], 1.0 op_sel_hi:[1,0]
	v_rcp_f32_e32 v60, v56
	v_rcp_f32_e32 v61, v57
	v_rcp_f32_e32 v62, v58
	v_rcp_f32_e32 v63, v59
	v_pk_fma_f32 v[28:29], v[56:57], v[60:61], 1.0 op_sel_hi:[1,1,0] neg_lo:[1,0,0] neg_hi:[1,0,0]
	v_pk_fma_f32 v[30:31], v[58:59], v[62:63], 1.0 op_sel_hi:[1,1,0] neg_lo:[1,0,0] neg_hi:[1,0,0]
	v_pk_fma_f32 v[60:61], v[28:29], v[60:61], v[60:61]
	v_pk_fma_f32 v[62:63], v[30:31], v[62:63], v[62:63]
	v_pk_fma_f32 v[28:29], v[56:57], v[60:61], 1.0 op_sel_hi:[1,1,0] neg_lo:[1,0,0] neg_hi:[1,0,0]
	v_pk_fma_f32 v[30:31], v[58:59], v[62:63], 1.0 op_sel_hi:[1,1,0] neg_lo:[1,0,0] neg_hi:[1,0,0]
	v_pk_fma_f32 v[64:65], v[28:29], v[60:61], v[60:61]
	v_pk_fma_f32 v[66:67], v[30:31], v[62:63], v[62:63]
	v_pk_fma_f32 v[28:29], v[56:57], v[64:65], 1.0 op_sel_hi:[1,1,0] neg_lo:[1,0,0] neg_hi:[1,0,0]
	v_pk_fma_f32 v[30:31], v[58:59], v[66:67], 1.0 op_sel_hi:[1,1,0] neg_lo:[1,0,0] neg_hi:[1,0,0]
	v_pk_fma_f32 v[28:29], v[28:29], v[60:61], v[64:65]
	v_pk_fma_f32 v[30:31], v[30:31], v[62:63], v[66:67]
	v_div_fixup_f32 v28, v28, v56, 1.0
	v_div_fixup_f32 v29, v29, v57, 1.0
	v_div_fixup_f32 v30, v30, v58, 1.0
	v_div_fixup_f32 v31, v31, v59, 1.0
	v_pk_mul_f32 v[14:15], v[14:15], v[28:29]
	v_pk_mul_f32 v[16:17], v[16:17], v[30:31]
	v_pk_mul_f32 v[10:11], v[10:11], s[100:101] op_sel_hi:[1,0]
	v_pk_mul_f32 v[12:13], v[12:13], s[100:101] op_sel_hi:[1,0]
	v_pk_mul_f32 v[14:15], v[14:15], s[100:101] op_sel_hi:[1,0]
	v_pk_mul_f32 v[16:17], v[16:17], s[100:101] op_sel_hi:[1,0]
	v_med3_f32 v10, v10, s86, v202
	v_med3_f32 v11, v11, s86, v202
	v_med3_f32 v12, v12, s86, v202
	v_med3_f32 v13, v13, s86, v202
	v_med3_f32 v14, v14, s86, v202
	v_med3_f32 v15, v15, s86, v202
	v_med3_f32 v16, v16, s86, v202
	v_med3_f32 v17, v17, s86, v202
	v_mov_b32_e32 v20, v6
	v_mov_b32_e32 v21, 0
	v_cvt_pk_fp8_f32 v26, v10, v11
	v_cvt_pk_fp8_f32 v27, v14, v15
	v_lshlrev_b64 v[20:21], 10, v[20:21]
	v_cvt_pk_fp8_f32 v26, v12, v13 op_sel:[0,0,1]
	v_cvt_pk_fp8_f32 v27, v16, v17 op_sel:[0,0,1]
	v_lshl_add_u64 v[20:21], v[4:5], 0, v[20:21]
	s_nop 0
	global_store_dwordx2 v[20:21], v[26:27], off
	v_add_u32_e32 v9, 32, v6
	v_lshl_add_u32 v7, v9, 8, v8
	ds_read_b128 v[22:25], v7
	s_waitcnt vmcnt(3) lgkmcnt(0)
; #define LAS __attribute__((address_space(3)))
; __device__ __forceinline__ float sigmoidf_(float x) { return 1.f / (1.f + __expf(-x)); }
; __device__ __forceinline__ unsigned pk4_fp8c(float a, float b, float c, float d) { return pk4_fp8(__builtin_amdgcn_fmed3f(a, -448.f, 448.f), __builtin_amdgcn_fmed3f(b, -448.f, 448.f), __builtin_amdgcn_fmed3f(c, -448.f, 448.f), __builtin_amdgcn_fmed3f(d, -448.f, 448.f)); }
; __device__ __forceinline__ void out_unit_m(LAS unsigned char* lds, LAS unsigned char* ldstab, const OutArgs a, const int wv) {
;     ...
;     for (int id = tid; id < 128 * 16; id += 512) { const int row = id >> 4, ch = id & 15;
;         const u32x4 y = *(const LAS u32x4*)(lds + row * TP + ch * 16); const u32x4 g = *(const u32x4*)(a.G + (size_t)row * a.ldg + 8 * ch);
;         const f32x4 g0 = *(const f32x4*)(a.gain + 8 * ch), g1 = *(const f32x4*)(a.gain + 8 * ch + 4);
;         const float yv[8] = {bf_lo(y.x), bf_hi(y.x), bf_lo(y.y), bf_hi(y.y), bf_lo(y.z), bf_hi(y.z), bf_lo(y.w), bf_hi(y.w)};
;         const float gv[8] = {bf_lo(g.x), bf_hi(g.x), bf_lo(g.y), bf_hi(g.y), bf_lo(g.z), bf_hi(g.z), bf_lo(g.w), bf_hi(g.w)};
;         const float gn[8] = {g0[0], g0[1], g0[2], g0[3], g1[0], g1[1], g1[2], g1[3]};
;         float ov[8];
; #pragma unroll
;         for (int i = 0; i < 8; ++i) ov[i] = yv[i] * gn[i] * sigmoidf_(gv[i]);
;         u32x2 w; w.x = pg8::pk4_fp8c(ov[0] * a.oscale, ov[1] * a.oscale, ov[2] * a.oscale, ov[3] * a.oscale); w.y = pg8::pk4_fp8c(ov[4] * a.oscale, ov[5] * a.oscale, ov[6] * a.oscale, ov[7] * a.oscale);
;         *(u32x2*)(a.Out + (size_t)row * a.ldo + 8 * ch) = w; }
	v_lshlrev_b32_e32 v10, 16, v22
	v_and_b32_e32 v11, 0xffff0000, v22
	v_lshlrev_b32_e32 v12, 16, v23
	v_and_b32_e32 v13, 0xffff0000, v23
	v_lshlrev_b32_e32 v14, 16, v24
	v_and_b32_e32 v15, 0xffff0000, v24
	v_lshlrev_b32_e32 v16, 16, v25
	v_and_b32_e32 v17, 0xffff0000, v25
	v_pk_mul_f32 v[10:11], v[32:33], v[10:11]
	v_pk_mul_f32 v[12:13], v[34:35], v[12:13]
	v_pk_mul_f32 v[14:15], v[36:37], v[14:15]
	v_pk_mul_f32 v[16:17], v[38:39], v[16:17]
	v_lshlrev_b32_e32 v56, 16, v44
	v_and_b32_e32 v57, 0xffff0000, v44
	v_lshlrev_b32_e32 v58, 16, v45
	v_and_b32_e32 v59, 0xffff0000, v45
	v_pk_mul_f32 v[56:57], v[56:57], s[98:99] op_sel_hi:[1,0]
	v_pk_mul_f32 v[58:59], v[58:59], s[98:99] op_sel_hi:[1,0]
	v_exp_f32_e32 v56, v56
	v_exp_f32_e32 v57, v57
	v_exp_f32_e32 v58, v58
	v_exp_f32_e32 v59, v59
	v_pk_add_f32 v[56:57], v[56:57], 1.0 op_sel_hi:[1,0]
	v_pk_add_f32 v[58:59], v[58:59], 1.0 op_sel_hi:[1,0]
	v_rcp_f32_e32 v60, v56
	v_rcp_f32_e32 v61, v57
	v_rcp_f32_e32 v62, v58
	v_rcp_f32_e32 v63, v59
	v_pk_fma_f32 v[28:29], v[56:57], v[60:61], 1.0 op_sel_hi:[1,1,0] neg_lo:[1,0,0] neg_hi:[1,0,0]
	v_pk_fma_f32 v[30:31], v[58:59], v[62:63], 1.0 op_sel_hi:[1,1,0] neg_lo:[1,0,0] neg_hi:[1,0,0]
	v_pk_fma_f32 v[60:61], v[28:29], v[60:61], v[60:61]
	v_pk_fma_f32 v[62:63], v[30:31], v[62:63], v[62:63]
	v_pk_fma_f32 v[28:29], v[56:57], v[60:61], 1.0 op_sel_hi:[1,1,0] neg_lo:[1,0,0] neg_hi:[1,0,0]
	v_pk_fma_f32 v[30:31], v[58:59], v[62:63], 1.0 op_sel_hi:[1,1,0] neg_lo:[1,0,0] neg_hi:[1,0,0]
	v_pk_fma_f32 v[64:65], v[28:29], v[60:61], v[60:61]
	v_pk_fma_f32 v[66:67], v[30:31], v[62:63], v[62:63]
	v_pk_fma_f32 v[28:29], v[56:57], v[64:65], 1.0 op_sel_hi:[1,1,0] neg_lo:[1,0,0] neg_hi:[1,0,0]
	v_pk_fma_f32 v[30:31], v[58:59], v[66:67], 1.0 op_sel_hi:[1,1,0] neg_lo:[1,0,0] neg_hi:[1,0,0]
	v_pk_fma_f32 v[28:29], v[28:29], v[60:61], v[64:65]
	v_pk_fma_f32 v[30:31], v[30:31], v[62:63], v[66:67]
	v_div_fixup_f32 v28, v28, v56, 1.0
	v_div_fixup_f32 v29, v29, v57, 1.0
	v_div_fixup_f32 v30, v30, v58, 1.0
	v_div_fixup_f32 v31, v31, v59, 1.0
	v_pk_mul_f32 v[10:11], v[10:11], v[28:29]
	v_pk_mul_f32 v[12:13], v[12:13], v[30:31]
	v_lshlrev_b32_e32 v56, 16, v46
	v_and_b32_e32 v57, 0xffff0000, v46
	v_lshlrev_b32_e32 v58, 16, v47
	v_and_b32_e32 v59, 0xffff0000, v47
	v_pk_mul_f32 v[56:57], v[56:57], s[98:99] op_sel_hi:[1,0]
	v_pk_mul_f32 v[58:59], v[58:59], s[98:99] op_sel_hi:[1,0]
	v_exp_f32_e32 v56, v56
	v_exp_f32_e32 v57, v57
	v_exp_f32_e32 v58, v58
	v_exp_f32_e32 v59, v59
	v_pk_add_f32 v[56:57], v[56:57], 1.0 op_sel_hi:[1,0]
	v_pk_add_f32 v[58:59], v[58:59], 1.0 op_sel_hi:[1,0]
	v_rcp_f32_e32 v60, v56
	v_rcp_f32_e32 v61, v57
	v_rcp_f32_e32 v62, v58
	v_rcp_f32_e32 v63, v59
	v_pk_fma_f32 v[28:29], v[56:57], v[60:61], 1.0 op_sel_hi:[1,1,0] neg_lo:[1,0,0] neg_hi:[1,0,0]
	v_pk_fma_f32 v[30:31], v[58:59], v[62:63], 1.0 op_sel_hi:[1,1,0] neg_lo:[1,0,0] neg_hi:[1,0,0]
	v_pk_fma_f32 v[60:61], v[28:29], v[60:61], v[60:61]
	v_pk_fma_f32 v[62:63], v[30:31], v[62:63], v[62:63]
	v_pk_fma_f32 v[28:29], v[56:57], v[60:61], 1.0 op_sel_hi:[1,1,0] neg_lo:[1,0,0] neg_hi:[1,0,0]
	v_pk_fma_f32 v[30:31], v[58:59], v[62:63], 1.0 op_sel_hi:[1,1,0] neg_lo:[1,0,0] neg_hi:[1,0,0]
	v_pk_fma_f32 v[64:65], v[28:29], v[60:61], v[60:61]
	v_pk_fma_f32 v[66:67], v[30:31], v[62:63], v[62:63]
	v_pk_fma_f32 v[28:29], v[56:57], v[64:65], 1.0 op_sel_hi:[1,1,0] neg_lo:[1,0,0] neg_hi:[1,0,0]
	v_pk_fma_f32 v[30:31], v[58:59], v[66:67], 1.0 op_sel_hi:[1,1,0] neg_lo:[1,0,0] neg_hi:[1,0,0]
	v_pk_fma_f32 v[28:29], v[28:29], v[60:61], v[64:65]
	v_pk_fma_f32 v[30:31], v[30:31], v[62:63], v[66:67]
	v_div_fixup_f32 v28, v28, v56, 1.0
	v_div_fixup_f32 v29, v29, v57, 1.0
	v_div_fixup_f32 v30, v30, v58, 1.0
	v_div_fixup_f32 v31, v31, v59, 1.0
	v_pk_mul_f32 v[14:15], v[14:15], v[28:29]
	v_pk_mul_f32 v[16:17], v[16:17], v[30:31]
	v_pk_mul_f32 v[10:11], v[10:11], s[100:101] op_sel_hi:[1,0]
	v_pk_mul_f32 v[12:13], v[12:13], s[100:101] op_sel_hi:[1,0]
	v_pk_mul_f32 v[14:15], v[14:15], s[100:101] op_sel_hi:[1,0]
	v_pk_mul_f32 v[16:17], v[16:17], s[100:101] op_sel_hi:[1,0]
	v_med3_f32 v10, v10, s86, v202
	v_med3_f32 v11, v11, s86, v202
	v_med3_f32 v12, v12, s86, v202
	v_med3_f32 v13, v13, s86, v202
	v_med3_f32 v14, v14, s86, v202
	v_med3_f32 v15, v15, s86, v202
	v_med3_f32 v16, v16, s86, v202
	v_med3_f32 v17, v17, s86, v202
	v_add_u32_e32 v20, 32, v6
	v_mov_b32_e32 v21, 0
	v_cvt_pk_fp8_f32 v26, v10, v11
	v_cvt_pk_fp8_f32 v27, v14, v15
	v_lshlrev_b64 v[20:21], 10, v[20:21]
	v_cvt_pk_fp8_f32 v26, v12, v13 op_sel:[0,0,1]
	v_cvt_pk_fp8_f32 v27, v16, v17 op_sel:[0,0,1]
	v_lshl_add_u64 v[20:21], v[4:5], 0, v[20:21]
	s_nop 0
	global_store_dwordx2 v[20:21], v[26:27], off
	v_add_u32_e32 v9, 64, v6
	v_lshl_add_u32 v7, v9, 8, v8
	ds_read_b128 v[22:25], v7
	s_waitcnt vmcnt(3) lgkmcnt(0)
; #define LAS __attribute__((address_space(3)))
; __device__ __forceinline__ float sigmoidf_(float x) { return 1.f / (1.f + __expf(-x)); }
; __device__ __forceinline__ unsigned pk4_fp8c(float a, float b, float c, float d) { return pk4_fp8(__builtin_amdgcn_fmed3f(a, -448.f, 448.f), __builtin_amdgcn_fmed3f(b, -448.f, 448.f), __builtin_amdgcn_fmed3f(c, -448.f, 448.f), __builtin_amdgcn_fmed3f(d, -448.f, 448.f)); }
; __device__ __forceinline__ void out_unit_m(LAS unsigned char* lds, LAS unsigned char* ldstab, const OutArgs a, const int wv) {
;     ...
;     for (int id = tid; id < 128 * 16; id += 512) { const int row = id >> 4, ch = id & 15;
;         const u32x4 y = *(const LAS u32x4*)(lds + row * TP + ch * 16); const u32x4 g = *(const u32x4*)(a.G + (size_t)row * a.ldg + 8 * ch);
;         const f32x4 g0 = *(const f32x4*)(a.gain + 8 * ch), g1 = *(const f32x4*)(a.gain + 8 * ch + 4);
;         const float yv[8] = {bf_lo(y.x), bf_hi(y.x), bf_lo(y.y), bf_hi(y.y), bf_lo(y.z), bf_hi(y.z), bf_lo(y.w), bf_hi(y.w)};
;         const float gv[8] = {bf_lo(g.x), bf_hi(g.x), bf_lo(g.y), bf_hi(g.y), bf_lo(g.z), bf_hi(g.z), bf_lo(g.w), bf_hi(g.w)};
;         const float gn[8] = {g0[0], g0[1], g0[2], g0[3], g1[0], g1[1], g1[2], g1[3]};
;         float ov[8];
; #pragma unroll
;         for (int i = 0; i < 8; ++i) ov[i] = yv[i] * gn[i] * sigmoidf_(gv[i]);
;         u32x2 w; w.x = pg8::pk4_fp8c(ov[0] * a.oscale, ov[1] * a.oscale, ov[2] * a.oscale, ov[3] * a.oscale); w.y = pg8::pk4_fp8c(ov[4] * a.oscale, ov[5] * a.oscale, ov[6] * a.oscale, ov[7] * a.oscale);
;         *(u32x2*)(a.Out + (size_t)row * a.ldo + 8 * ch) = w; }
	v_lshlrev_b32_e32 v10, 16, v22
	v_and_b32_e32 v11, 0xffff0000, v22
	v_lshlrev_b32_e32 v12, 16, v23
	v_and_b32_e32 v13, 0xffff0000, v23
	v_lshlrev_b32_e32 v14, 16, v24
	v_and_b32_e32 v15, 0xffff0000, v24
	v_lshlrev_b32_e32 v16, 16, v25
	v_and_b32_e32 v17, 0xffff0000, v25
	v_pk_mul_f32 v[10:11], v[32:33], v[10:11]
	v_pk_mul_f32 v[12:13], v[34:35], v[12:13]
	v_pk_mul_f32 v[14:15], v[36:37], v[14:15]
	v_pk_mul_f32 v[16:17], v[38:39], v[16:17]
	v_lshlrev_b32_e32 v56, 16, v48
	v_and_b32_e32 v57, 0xffff0000, v48
	v_lshlrev_b32_e32 v58, 16, v49
	v_and_b32_e32 v59, 0xffff0000, v49
	v_pk_mul_f32 v[56:57], v[56:57], s[98:99] op_sel_hi:[1,0]
	v_pk_mul_f32 v[58:59], v[58:59], s[98:99] op_sel_hi:[1,0]
	v_exp_f32_e32 v56, v56
	v_exp_f32_e32 v57, v57
	v_exp_f32_e32 v58, v58
	v_exp_f32_e32 v59, v59
	v_pk_add_f32 v[56:57], v[56:57], 1.0 op_sel_hi:[1,0]
	v_pk_add_f32 v[58:59], v[58:59], 1.0 op_sel_hi:[1,0]
	v_rcp_f32_e32 v60, v56
	v_rcp_f32_e32 v61, v57
	v_rcp_f32_e32 v62, v58
	v_rcp_f32_e32 v63, v59
	v_pk_fma_f32 v[28:29], v[56:57], v[60:61], 1.0 op_sel_hi:[1,1,0] neg_lo:[1,0,0] neg_hi:[1,0,0]
	v_pk_fma_f32 v[30:31], v[58:59], v[62:63], 1.0 op_sel_hi:[1,1,0] neg_lo:[1,0,0] neg_hi:[1,0,0]
	v_pk_fma_f32 v[60:61], v[28:29], v[60:61], v[60:61]
	v_pk_fma_f32 v[62:63], v[30:31], v[62:63], v[62:63]
	v_pk_fma_f32 v[28:29], v[56:57], v[60:61], 1.0 op_sel_hi:[1,1,0] neg_lo:[1,0,0] neg_hi:[1,0,0]
	v_pk_fma_f32 v[30:31], v[58:59], v[62:63], 1.0 op_sel_hi:[1,1,0] neg_lo:[1,0,0] neg_hi:[1,0,0]
	v_pk_fma_f32 v[64:65], v[28:29], v[60:61], v[60:61]
	v_pk_fma_f32 v[66:67], v[30:31], v[62:63], v[62:63]
	v_pk_fma_f32 v[28:29], v[56:57], v[64:65], 1.0 op_sel_hi:[1,1,0] neg_lo:[1,0,0] neg_hi:[1,0,0]
	v_pk_fma_f32 v[30:31], v[58:59], v[66:67], 1.0 op_sel_hi:[1,1,0] neg_lo:[1,0,0] neg_hi:[1,0,0]
	v_pk_fma_f32 v[28:29], v[28:29], v[60:61], v[64:65]
	v_pk_fma_f32 v[30:31], v[30:31], v[62:63], v[66:67]
	v_div_fixup_f32 v28, v28, v56, 1.0
	v_div_fixup_f32 v29, v29, v57, 1.0
	v_div_fixup_f32 v30, v30, v58, 1.0
	v_div_fixup_f32 v31, v31, v59, 1.0
	v_pk_mul_f32 v[10:11], v[10:11], v[28:29]
	v_pk_mul_f32 v[12:13], v[12:13], v[30:31]
	v_lshlrev_b32_e32 v56, 16, v50
	v_and_b32_e32 v57, 0xffff0000, v50
	v_lshlrev_b32_e32 v58, 16, v51
	v_and_b32_e32 v59, 0xffff0000, v51
	v_pk_mul_f32 v[56:57], v[56:57], s[98:99] op_sel_hi:[1,0]
	v_pk_mul_f32 v[58:59], v[58:59], s[98:99] op_sel_hi:[1,0]
	v_exp_f32_e32 v56, v56
	v_exp_f32_e32 v57, v57
	v_exp_f32_e32 v58, v58
	v_exp_f32_e32 v59, v59
	v_pk_add_f32 v[56:57], v[56:57], 1.0 op_sel_hi:[1,0]
	v_pk_add_f32 v[58:59], v[58:59], 1.0 op_sel_hi:[1,0]
	v_rcp_f32_e32 v60, v56
	v_rcp_f32_e32 v61, v57
	v_rcp_f32_e32 v62, v58
	v_rcp_f32_e32 v63, v59
	v_pk_fma_f32 v[28:29], v[56:57], v[60:61], 1.0 op_sel_hi:[1,1,0] neg_lo:[1,0,0] neg_hi:[1,0,0]
	v_pk_fma_f32 v[30:31], v[58:59], v[62:63], 1.0 op_sel_hi:[1,1,0] neg_lo:[1,0,0] neg_hi:[1,0,0]
	v_pk_fma_f32 v[60:61], v[28:29], v[60:61], v[60:61]
	v_pk_fma_f32 v[62:63], v[30:31], v[62:63], v[62:63]
	v_pk_fma_f32 v[28:29], v[56:57], v[60:61], 1.0 op_sel_hi:[1,1,0] neg_lo:[1,0,0] neg_hi:[1,0,0]
	v_pk_fma_f32 v[30:31], v[58:59], v[62:63], 1.0 op_sel_hi:[1,1,0] neg_lo:[1,0,0] neg_hi:[1,0,0]
	v_pk_fma_f32 v[64:65], v[28:29], v[60:61], v[60:61]
	v_pk_fma_f32 v[66:67], v[30:31], v[62:63], v[62:63]
	v_pk_fma_f32 v[28:29], v[56:57], v[64:65], 1.0 op_sel_hi:[1,1,0] neg_lo:[1,0,0] neg_hi:[1,0,0]
	v_pk_fma_f32 v[30:31], v[58:59], v[66:67], 1.0 op_sel_hi:[1,1,0] neg_lo:[1,0,0] neg_hi:[1,0,0]
	v_pk_fma_f32 v[28:29], v[28:29], v[60:61], v[64:65]
	v_pk_fma_f32 v[30:31], v[30:31], v[62:63], v[66:67]
	v_div_fixup_f32 v28, v28, v56, 1.0
	v_div_fixup_f32 v29, v29, v57, 1.0
	v_div_fixup_f32 v30, v30, v58, 1.0
	v_div_fixup_f32 v31, v31, v59, 1.0
	v_pk_mul_f32 v[14:15], v[14:15], v[28:29]
	v_pk_mul_f32 v[16:17], v[16:17], v[30:31]
	v_pk_mul_f32 v[10:11], v[10:11], s[100:101] op_sel_hi:[1,0]
	v_pk_mul_f32 v[12:13], v[12:13], s[100:101] op_sel_hi:[1,0]
	v_pk_mul_f32 v[14:15], v[14:15], s[100:101] op_sel_hi:[1,0]
	v_pk_mul_f32 v[16:17], v[16:17], s[100:101] op_sel_hi:[1,0]
	v_med3_f32 v10, v10, s86, v202
	v_med3_f32 v11, v11, s86, v202
	v_med3_f32 v12, v12, s86, v202
	v_med3_f32 v13, v13, s86, v202
	v_med3_f32 v14, v14, s86, v202
	v_med3_f32 v15, v15, s86, v202
	v_med3_f32 v16, v16, s86, v202
	v_med3_f32 v17, v17, s86, v202
	v_add_u32_e32 v20, 64, v6
	v_mov_b32_e32 v21, 0
	v_cvt_pk_fp8_f32 v26, v10, v11
	v_cvt_pk_fp8_f32 v27, v14, v15
	v_lshlrev_b64 v[20:21], 10, v[20:21]
	v_cvt_pk_fp8_f32 v26, v12, v13 op_sel:[0,0,1]
	v_cvt_pk_fp8_f32 v27, v16, v17 op_sel:[0,0,1]
	v_lshl_add_u64 v[20:21], v[4:5], 0, v[20:21]
	s_nop 0
	global_store_dwordx2 v[20:21], v[26:27], off
	v_add_u32_e32 v9, 96, v6
	v_lshl_add_u32 v7, v9, 8, v8
	ds_read_b128 v[22:25], v7
	s_waitcnt vmcnt(3) lgkmcnt(0)
; #define LAS __attribute__((address_space(3)))
; __device__ __forceinline__ float sigmoidf_(float x) { return 1.f / (1.f + __expf(-x)); }
; __device__ __forceinline__ unsigned pk4_fp8c(float a, float b, float c, float d) { return pk4_fp8(__builtin_amdgcn_fmed3f(a, -448.f, 448.f), __builtin_amdgcn_fmed3f(b, -448.f, 448.f), __builtin_amdgcn_fmed3f(c, -448.f, 448.f), __builtin_amdgcn_fmed3f(d, -448.f, 448.f)); }
; __device__ __forceinline__ void out_unit_m(LAS unsigned char* lds, LAS unsigned char* ldstab, const OutArgs a, const int wv) {
;     ...
;     for (int id = tid; id < 128 * 16; id += 512) { const int row = id >> 4, ch = id & 15;
;         const u32x4 y = *(const LAS u32x4*)(lds + row * TP + ch * 16); const u32x4 g = *(const u32x4*)(a.G + (size_t)row * a.ldg + 8 * ch);
;         const f32x4 g0 = *(const f32x4*)(a.gain + 8 * ch), g1 = *(const f32x4*)(a.gain + 8 * ch + 4);
;         const float yv[8] = {bf_lo(y.x), bf_hi(y.x), bf_lo(y.y), bf_hi(y.y), bf_lo(y.z), bf_hi(y.z), bf_lo(y.w), bf_hi(y.w)};
;         const float gv[8] = {bf_lo(g.x), bf_hi(g.x), bf_lo(g.y), bf_hi(g.y), bf_lo(g.z), bf_hi(g.z), bf_lo(g.w), bf_hi(g.w)};
;         const float gn[8] = {g0[0], g0[1], g0[2], g0[3], g1[0], g1[1], g1[2], g1[3]};
;         float ov[8];
; #pragma unroll
;         for (int i = 0; i < 8; ++i) ov[i] = yv[i] * gn[i] * sigmoidf_(gv[i]);
;         u32x2 w; w.x = pg8::pk4_fp8c(ov[0] * a.oscale, ov[1] * a.oscale, ov[2] * a.oscale, ov[3] * a.oscale); w.y = pg8::pk4_fp8c(ov[4] * a.oscale, ov[5] * a.oscale, ov[6] * a.oscale, ov[7] * a.oscale);
;         *(u32x2*)(a.Out + (size_t)row * a.ldo + 8 * ch) = w; }
	v_lshlrev_b32_e32 v10, 16, v22
	v_and_b32_e32 v11, 0xffff0000, v22
	v_lshlrev_b32_e32 v12, 16, v23
	v_and_b32_e32 v13, 0xffff0000, v23
	v_lshlrev_b32_e32 v14, 16, v24
	v_and_b32_e32 v15, 0xffff0000, v24
	v_lshlrev_b32_e32 v16, 16, v25
	v_and_b32_e32 v17, 0xffff0000, v25
	v_pk_mul_f32 v[10:11], v[32:33], v[10:11]
	v_pk_mul_f32 v[12:13], v[34:35], v[12:13]
	v_pk_mul_f32 v[14:15], v[36:37], v[14:15]
	v_pk_mul_f32 v[16:17], v[38:39], v[16:17]
	v_lshlrev_b32_e32 v56, 16, v52
	v_and_b32_e32 v57, 0xffff0000, v52
	v_lshlrev_b32_e32 v58, 16, v53
	v_and_b32_e32 v59, 0xffff0000, v53
	v_pk_mul_f32 v[56:57], v[56:57], s[98:99] op_sel_hi:[1,0]
	v_pk_mul_f32 v[58:59], v[58:59], s[98:99] op_sel_hi:[1,0]
	v_exp_f32_e32 v56, v56
	v_exp_f32_e32 v57, v57
	v_exp_f32_e32 v58, v58
	v_exp_f32_e32 v59, v59
	v_pk_add_f32 v[56:57], v[56:57], 1.0 op_sel_hi:[1,0]
	v_pk_add_f32 v[58:59], v[58:59], 1.0 op_sel_hi:[1,0]
	v_rcp_f32_e32 v60, v56
	v_rcp_f32_e32 v61, v57
	v_rcp_f32_e32 v62, v58
	v_rcp_f32_e32 v63, v59
	v_pk_fma_f32 v[28:29], v[56:57], v[60:61], 1.0 op_sel_hi:[1,1,0] neg_lo:[1,0,0] neg_hi:[1,0,0]
	v_pk_fma_f32 v[30:31], v[58:59], v[62:63], 1.0 op_sel_hi:[1,1,0] neg_lo:[1,0,0] neg_hi:[1,0,0]
	v_pk_fma_f32 v[60:61], v[28:29], v[60:61], v[60:61]
	v_pk_fma_f32 v[62:63], v[30:31], v[62:63], v[62:63]
	v_pk_fma_f32 v[28:29], v[56:57], v[60:61], 1.0 op_sel_hi:[1,1,0] neg_lo:[1,0,0] neg_hi:[1,0,0]
	v_pk_fma_f32 v[30:31], v[58:59], v[62:63], 1.0 op_sel_hi:[1,1,0] neg_lo:[1,0,0] neg_hi:[1,0,0]
	v_pk_fma_f32 v[64:65], v[28:29], v[60:61], v[60:61]
	v_pk_fma_f32 v[66:67], v[30:31], v[62:63], v[62:63]
	v_pk_fma_f32 v[28:29], v[56:57], v[64:65], 1.0 op_sel_hi:[1,1,0] neg_lo:[1,0,0] neg_hi:[1,0,0]
	v_pk_fma_f32 v[30:31], v[58:59], v[66:67], 1.0 op_sel_hi:[1,1,0] neg_lo:[1,0,0] neg_hi:[1,0,0]
	v_pk_fma_f32 v[28:29], v[28:29], v[60:61], v[64:65]
	v_pk_fma_f32 v[30:31], v[30:31], v[62:63], v[66:67]
	v_div_fixup_f32 v28, v28, v56, 1.0
	v_div_fixup_f32 v29, v29, v57, 1.0
	v_div_fixup_f32 v30, v30, v58, 1.0
	v_div_fixup_f32 v31, v31, v59, 1.0
	v_pk_mul_f32 v[10:11], v[10:11], v[28:29]
	v_pk_mul_f32 v[12:13], v[12:13], v[30:31]
	v_lshlrev_b32_e32 v56, 16, v54
	v_and_b32_e32 v57, 0xffff0000, v54
	v_lshlrev_b32_e32 v58, 16, v55
	v_and_b32_e32 v59, 0xffff0000, v55
	v_pk_mul_f32 v[56:57], v[56:57], s[98:99] op_sel_hi:[1,0]
	v_pk_mul_f32 v[58:59], v[58:59], s[98:99] op_sel_hi:[1,0]
	v_exp_f32_e32 v56, v56
	v_exp_f32_e32 v57, v57
	v_exp_f32_e32 v58, v58
	v_exp_f32_e32 v59, v59
	v_pk_add_f32 v[56:57], v[56:57], 1.0 op_sel_hi:[1,0]
	v_pk_add_f32 v[58:59], v[58:59], 1.0 op_sel_hi:[1,0]
	v_rcp_f32_e32 v60, v56
	v_rcp_f32_e32 v61, v57
	v_rcp_f32_e32 v62, v58
	v_rcp_f32_e32 v63, v59
	v_pk_fma_f32 v[28:29], v[56:57], v[60:61], 1.0 op_sel_hi:[1,1,0] neg_lo:[1,0,0] neg_hi:[1,0,0]
	v_pk_fma_f32 v[30:31], v[58:59], v[62:63], 1.0 op_sel_hi:[1,1,0] neg_lo:[1,0,0] neg_hi:[1,0,0]
	v_pk_fma_f32 v[60:61], v[28:29], v[60:61], v[60:61]
	v_pk_fma_f32 v[62:63], v[30:31], v[62:63], v[62:63]
	v_pk_fma_f32 v[28:29], v[56:57], v[60:61], 1.0 op_sel_hi:[1,1,0] neg_lo:[1,0,0] neg_hi:[1,0,0]
	v_pk_fma_f32 v[30:31], v[58:59], v[62:63], 1.0 op_sel_hi:[1,1,0] neg_lo:[1,0,0] neg_hi:[1,0,0]
	v_pk_fma_f32 v[64:65], v[28:29], v[60:61], v[60:61]
	v_pk_fma_f32 v[66:67], v[30:31], v[62:63], v[62:63]
	v_pk_fma_f32 v[28:29], v[56:57], v[64:65], 1.0 op_sel_hi:[1,1,0] neg_lo:[1,0,0] neg_hi:[1,0,0]
	v_pk_fma_f32 v[30:31], v[58:59], v[66:67], 1.0 op_sel_hi:[1,1,0] neg_lo:[1,0,0] neg_hi:[1,0,0]
	v_pk_fma_f32 v[28:29], v[28:29], v[60:61], v[64:65]
	v_pk_fma_f32 v[30:31], v[30:31], v[62:63], v[66:67]
	v_div_fixup_f32 v28, v28, v56, 1.0
	v_div_fixup_f32 v29, v29, v57, 1.0
	v_div_fixup_f32 v30, v30, v58, 1.0
	v_div_fixup_f32 v31, v31, v59, 1.0
	v_pk_mul_f32 v[14:15], v[14:15], v[28:29]
	v_pk_mul_f32 v[16:17], v[16:17], v[30:31]
	v_pk_mul_f32 v[10:11], v[10:11], s[100:101] op_sel_hi:[1,0]
	v_pk_mul_f32 v[12:13], v[12:13], s[100:101] op_sel_hi:[1,0]
	v_pk_mul_f32 v[14:15], v[14:15], s[100:101] op_sel_hi:[1,0]
	v_pk_mul_f32 v[16:17], v[16:17], s[100:101] op_sel_hi:[1,0]
	v_med3_f32 v10, v10, s86, v202
	v_med3_f32 v11, v11, s86, v202
	v_med3_f32 v12, v12, s86, v202
	v_med3_f32 v13, v13, s86, v202
	v_med3_f32 v14, v14, s86, v202
	v_med3_f32 v15, v15, s86, v202
	v_med3_f32 v16, v16, s86, v202
	v_med3_f32 v17, v17, s86, v202
	v_add_u32_e32 v20, 96, v6
	v_mov_b32_e32 v21, 0
	v_cvt_pk_fp8_f32 v26, v10, v11
	v_cvt_pk_fp8_f32 v27, v14, v15
	v_lshlrev_b64 v[20:21], 10, v[20:21]
	v_cvt_pk_fp8_f32 v26, v12, v13 op_sel:[0,0,1]
	v_cvt_pk_fp8_f32 v27, v16, v17 op_sel:[0,0,1]
	v_lshl_add_u64 v[20:21], v[4:5], 0, v[20:21]
	s_nop 0
	global_store_dwordx2 v[20:21], v[26:27], off
